# GEMM K-loops: removed the priority flip in the middle of each 32-MFMA block (kept the raise at block start and the drop at its end)
# speedup vs baseline: 1.0497x; 1.0012x over previous
.LBB0_823:
	s_add_u32 s48, s46, 0xfff80080
	s_addc_u32 s49, s47, -1
	s_add_i32 s69, 0, 0x10000
	s_cmp_eq_u32 s67, 28
	s_cselect_b32 s83, s31, s49
	s_cselect_b32 s82, s30, s48
	s_cselect_b32 s49, s45, s15
	s_cselect_b32 s48, s44, s14
	s_add_i32 s70, 0, 0x14000
	v_add_u32_e32 v156, s69, v171
	v_add_u32_e32 v168, s70, v171
	ds_read_b128 v[144:147], v156
	ds_read_b128 v[148:151], v156 offset:1024
	ds_read_b128 v[152:155], v156 offset:2048
	ds_read_b128 v[156:159], v156 offset:3072
	ds_read_b128 v[160:163], v168
	ds_read_b128 v[164:167], v168 offset:1024
	ds_read_b128 v[206:209], v168 offset:2048
	ds_read_b128 v[210:213], v168 offset:3072
	s_add_i32 m0, s55, 0xc000
	ds_read_b128 v[214:217], v189
	ds_read_b128 v[218:221], v189 offset:1024
	ds_read_b128 v[222:225], v189 offset:2048
	ds_read_b128 v[226:229], v189 offset:3072
	ds_read_b128 v[230:233], v189 offset:4096
	ds_read_b128 v[234:237], v189 offset:5120
	ds_read_b128 v[238:241], v189 offset:6144
	ds_read_b128 v[242:245], v189 offset:7168
	global_load_lds_dwordx4 v140, s[46:47]
	s_add_i32 m0, s55, 0xe000
	s_nop 0
	global_load_lds_dwordx4 v142, s[46:47]
	s_waitcnt vmcnt(8)
	s_waitcnt lgkmcnt(0)
	s_barrier
	s_setprio 1
	s_waitcnt lgkmcnt(0)
	v_mfma_f32_16x16x32_bf16 v[124:127], v[144:147], v[214:217], v[124:127]
	v_mfma_f32_16x16x32_bf16 v[120:123], v[152:155], v[214:217], v[120:123]
	v_mfma_f32_16x16x32_bf16 v[108:111], v[144:147], v[222:225], v[108:111]
	v_mfma_f32_16x16x32_bf16 v[104:107], v[152:155], v[222:225], v[104:107]
	v_mfma_f32_16x16x32_bf16 v[92:95], v[144:147], v[230:233], v[92:95]
	v_mfma_f32_16x16x32_bf16 v[88:91], v[152:155], v[230:233], v[88:91]
	v_mfma_f32_16x16x32_bf16 v[76:79], v[144:147], v[238:241], v[76:79]
	v_mfma_f32_16x16x32_bf16 v[72:75], v[152:155], v[238:241], v[72:75]
	v_mfma_f32_16x16x32_bf16 v[124:127], v[148:151], v[218:221], v[124:127]
	v_mfma_f32_16x16x32_bf16 v[120:123], v[156:159], v[218:221], v[120:123]
	v_mfma_f32_16x16x32_bf16 v[108:111], v[148:151], v[226:229], v[108:111]
	v_mfma_f32_16x16x32_bf16 v[104:107], v[156:159], v[226:229], v[104:107]
	v_mfma_f32_16x16x32_bf16 v[92:95], v[148:151], v[234:237], v[92:95]
	v_mfma_f32_16x16x32_bf16 v[88:91], v[156:159], v[234:237], v[88:91]
	v_mfma_f32_16x16x32_bf16 v[76:79], v[148:151], v[242:245], v[76:79]
	v_mfma_f32_16x16x32_bf16 v[72:75], v[156:159], v[242:245], v[72:75]
	v_mfma_f32_16x16x32_bf16 v[116:119], v[160:163], v[214:217], v[116:119]
	v_mfma_f32_16x16x32_bf16 v[112:115], v[206:209], v[214:217], v[112:115]
	v_mfma_f32_16x16x32_bf16 v[100:103], v[160:163], v[222:225], v[100:103]
	v_mfma_f32_16x16x32_bf16 v[96:99], v[206:209], v[222:225], v[96:99]
	v_mfma_f32_16x16x32_bf16 v[84:87], v[160:163], v[230:233], v[84:87]
	v_mfma_f32_16x16x32_bf16 v[80:83], v[206:209], v[230:233], v[80:83]
	v_mfma_f32_16x16x32_bf16 v[68:71], v[160:163], v[238:241], v[68:71]
	v_mfma_f32_16x16x32_bf16 v[64:67], v[206:209], v[238:241], v[64:67]
	v_mfma_f32_16x16x32_bf16 v[116:119], v[164:167], v[218:221], v[116:119]
	v_mfma_f32_16x16x32_bf16 v[112:115], v[210:213], v[218:221], v[112:115]
	v_mfma_f32_16x16x32_bf16 v[100:103], v[164:167], v[226:229], v[100:103]
	v_mfma_f32_16x16x32_bf16 v[96:99], v[210:213], v[226:229], v[96:99]
	v_mfma_f32_16x16x32_bf16 v[84:87], v[164:167], v[234:237], v[84:87]
	v_mfma_f32_16x16x32_bf16 v[80:83], v[210:213], v[234:237], v[80:83]
	v_mfma_f32_16x16x32_bf16 v[68:71], v[164:167], v[242:245], v[68:71]
	v_mfma_f32_16x16x32_bf16 v[64:67], v[210:213], v[242:245], v[64:67]
	s_setprio 0
	s_barrier
	s_add_i32 s69, s69, s23
	s_mov_b32 m0, s69
	ds_read_b128 v[214:217], v189 offset:16384
	ds_read_b128 v[218:221], v189 offset:17408
	ds_read_b128 v[222:225], v189 offset:18432
	ds_read_b128 v[226:229], v189 offset:19456
	ds_read_b128 v[230:233], v189 offset:20480
	ds_read_b128 v[234:237], v189 offset:21504
	ds_read_b128 v[238:241], v189 offset:22528
	ds_read_b128 v[242:245], v189 offset:23552
	global_load_lds_dwordx4 v130, s[48:49]
	s_add_i32 m0, s69, 0x2000
	s_add_u32 s84, s48, 0x80000
	s_addc_u32 s85, s49, 0
	s_add_i32 s69, s70, s23
	global_load_lds_dwordx4 v134, s[48:49]
	s_mov_b32 m0, s69
	s_nop 0
	global_load_lds_dwordx4 v130, s[84:85]
	s_add_i32 m0, s69, 0x2000
	s_nop 0
	global_load_lds_dwordx4 v134, s[84:85]
	s_mov_b32 m0, s55
	s_nop 0
	global_load_lds_dwordx4 v128, s[82:83]
	s_mov_b32 m0, s52
	s_nop 0
	global_load_lds_dwordx4 v132, s[82:83]
	s_waitcnt vmcnt(8)
	s_waitcnt lgkmcnt(0)
	s_barrier
	s_setprio 1
	s_waitcnt lgkmcnt(0)
	v_mfma_f32_16x16x32_bf16 v[60:63], v[144:147], v[214:217], v[60:63]
	v_mfma_f32_16x16x32_bf16 v[56:59], v[152:155], v[214:217], v[56:59]
	v_mfma_f32_16x16x32_bf16 v[44:47], v[144:147], v[222:225], v[44:47]
	v_mfma_f32_16x16x32_bf16 v[40:43], v[152:155], v[222:225], v[40:43]
	v_mfma_f32_16x16x32_bf16 v[28:31], v[144:147], v[230:233], v[28:31]
	v_mfma_f32_16x16x32_bf16 v[24:27], v[152:155], v[230:233], v[24:27]
	v_mfma_f32_16x16x32_bf16 v[12:15], v[144:147], v[238:241], v[12:15]
	v_mfma_f32_16x16x32_bf16 v[8:11], v[152:155], v[238:241], v[8:11]
	v_mfma_f32_16x16x32_bf16 v[60:63], v[148:151], v[218:221], v[60:63]
	v_mfma_f32_16x16x32_bf16 v[56:59], v[156:159], v[218:221], v[56:59]
	v_mfma_f32_16x16x32_bf16 v[44:47], v[148:151], v[226:229], v[44:47]
	v_mfma_f32_16x16x32_bf16 v[40:43], v[156:159], v[226:229], v[40:43]
	v_mfma_f32_16x16x32_bf16 v[28:31], v[148:151], v[234:237], v[28:31]
	v_mfma_f32_16x16x32_bf16 v[24:27], v[156:159], v[234:237], v[24:27]
	v_mfma_f32_16x16x32_bf16 v[12:15], v[148:151], v[242:245], v[12:15]
	v_mfma_f32_16x16x32_bf16 v[8:11], v[156:159], v[242:245], v[8:11]
	v_mfma_f32_16x16x32_bf16 v[52:55], v[160:163], v[214:217], v[52:55]
	v_mfma_f32_16x16x32_bf16 v[48:51], v[206:209], v[214:217], v[48:51]
	v_mfma_f32_16x16x32_bf16 v[36:39], v[160:163], v[222:225], v[36:39]
	v_mfma_f32_16x16x32_bf16 v[32:35], v[206:209], v[222:225], v[32:35]
	v_mfma_f32_16x16x32_bf16 v[20:23], v[160:163], v[230:233], v[20:23]
	v_mfma_f32_16x16x32_bf16 v[16:19], v[206:209], v[230:233], v[16:19]
	v_mfma_f32_16x16x32_bf16 v[4:7], v[160:163], v[238:241], v[4:7]
	v_mfma_f32_16x16x32_bf16 v[0:3], v[206:209], v[238:241], v[0:3]
	v_mfma_f32_16x16x32_bf16 v[52:55], v[164:167], v[218:221], v[52:55]
	v_mfma_f32_16x16x32_bf16 v[48:51], v[210:213], v[218:221], v[48:51]
	v_mfma_f32_16x16x32_bf16 v[36:39], v[164:167], v[226:229], v[36:39]
	v_mfma_f32_16x16x32_bf16 v[32:35], v[210:213], v[226:229], v[32:35]
	v_mfma_f32_16x16x32_bf16 v[20:23], v[164:167], v[234:237], v[20:23]
	v_mfma_f32_16x16x32_bf16 v[16:19], v[210:213], v[234:237], v[16:19]
	v_mfma_f32_16x16x32_bf16 v[4:7], v[164:167], v[242:245], v[4:7]
	v_mfma_f32_16x16x32_bf16 v[0:3], v[210:213], v[242:245], v[0:3]
	s_setprio 0
	s_barrier
	s_add_i32 s69, 0, 0x18000
	s_add_i32 s70, 0, 0x1c000
	v_add_u32_e32 v156, s69, v171
	v_add_u32_e32 v176, s70, v171
	ds_read_b128 v[144:147], v156
	ds_read_b128 v[148:151], v156 offset:1024
	ds_read_b128 v[152:155], v156 offset:2048
	ds_read_b128 v[156:159], v156 offset:3072
	ds_read_b128 v[160:163], v176
	ds_read_b128 v[164:167], v176 offset:1024
	ds_read_b128 v[206:209], v176 offset:2048
	ds_read_b128 v[210:213], v176 offset:3072
	s_add_u32 s82, s82, 0x80000
	s_addc_u32 s83, s83, 0
	s_mov_b32 m0, s53
	ds_read_b128 v[214:217], v189 offset:32768
	ds_read_b128 v[218:221], v189 offset:33792
	ds_read_b128 v[222:225], v189 offset:34816
	ds_read_b128 v[226:229], v189 offset:35840
	ds_read_b128 v[230:233], v189 offset:36864
	ds_read_b128 v[234:237], v189 offset:37888
	ds_read_b128 v[238:241], v189 offset:38912
	ds_read_b128 v[242:245], v189 offset:39936
	global_load_lds_dwordx4 v128, s[82:83]
	s_mov_b32 m0, s94
	s_nop 0
	global_load_lds_dwordx4 v132, s[82:83]
	s_waitcnt vmcnt(8)
	s_waitcnt lgkmcnt(0)
	s_barrier
	s_setprio 1
	s_waitcnt lgkmcnt(0)
	v_mfma_f32_16x16x32_bf16 v[124:127], v[144:147], v[214:217], v[124:127]
	v_mfma_f32_16x16x32_bf16 v[120:123], v[152:155], v[214:217], v[120:123]
	v_mfma_f32_16x16x32_bf16 v[108:111], v[144:147], v[222:225], v[108:111]
	v_mfma_f32_16x16x32_bf16 v[104:107], v[152:155], v[222:225], v[104:107]
	v_mfma_f32_16x16x32_bf16 v[92:95], v[144:147], v[230:233], v[92:95]
	v_mfma_f32_16x16x32_bf16 v[88:91], v[152:155], v[230:233], v[88:91]
	v_mfma_f32_16x16x32_bf16 v[76:79], v[144:147], v[238:241], v[76:79]
	v_mfma_f32_16x16x32_bf16 v[72:75], v[152:155], v[238:241], v[72:75]
	v_mfma_f32_16x16x32_bf16 v[124:127], v[148:151], v[218:221], v[124:127]
	v_mfma_f32_16x16x32_bf16 v[120:123], v[156:159], v[218:221], v[120:123]
	v_mfma_f32_16x16x32_bf16 v[108:111], v[148:151], v[226:229], v[108:111]
	v_mfma_f32_16x16x32_bf16 v[104:107], v[156:159], v[226:229], v[104:107]
	v_mfma_f32_16x16x32_bf16 v[92:95], v[148:151], v[234:237], v[92:95]
	v_mfma_f32_16x16x32_bf16 v[88:91], v[156:159], v[234:237], v[88:91]
	v_mfma_f32_16x16x32_bf16 v[76:79], v[148:151], v[242:245], v[76:79]
	v_mfma_f32_16x16x32_bf16 v[72:75], v[156:159], v[242:245], v[72:75]
	v_mfma_f32_16x16x32_bf16 v[116:119], v[160:163], v[214:217], v[116:119]
	v_mfma_f32_16x16x32_bf16 v[112:115], v[206:209], v[214:217], v[112:115]
	v_mfma_f32_16x16x32_bf16 v[100:103], v[160:163], v[222:225], v[100:103]
	v_mfma_f32_16x16x32_bf16 v[96:99], v[206:209], v[222:225], v[96:99]
	v_mfma_f32_16x16x32_bf16 v[84:87], v[160:163], v[230:233], v[84:87]
	v_mfma_f32_16x16x32_bf16 v[80:83], v[206:209], v[230:233], v[80:83]
	v_mfma_f32_16x16x32_bf16 v[68:71], v[160:163], v[238:241], v[68:71]
	v_mfma_f32_16x16x32_bf16 v[64:67], v[206:209], v[238:241], v[64:67]
	v_mfma_f32_16x16x32_bf16 v[116:119], v[164:167], v[218:221], v[116:119]
	v_mfma_f32_16x16x32_bf16 v[112:115], v[210:213], v[218:221], v[112:115]
	v_mfma_f32_16x16x32_bf16 v[100:103], v[164:167], v[226:229], v[100:103]
	v_mfma_f32_16x16x32_bf16 v[96:99], v[210:213], v[226:229], v[96:99]
	v_mfma_f32_16x16x32_bf16 v[84:87], v[164:167], v[234:237], v[84:87]
	v_mfma_f32_16x16x32_bf16 v[80:83], v[210:213], v[234:237], v[80:83]
	v_mfma_f32_16x16x32_bf16 v[68:71], v[164:167], v[242:245], v[68:71]
	v_mfma_f32_16x16x32_bf16 v[64:67], v[210:213], v[242:245], v[64:67]
	s_setprio 0
	s_barrier
	s_add_i32 s69, s69, s23
	s_mov_b32 m0, s69
	ds_read_b128 v[214:217], v189 offset:49152
	ds_read_b128 v[218:221], v189 offset:50176
	ds_read_b128 v[222:225], v189 offset:51200
	ds_read_b128 v[226:229], v189 offset:52224
	ds_read_b128 v[230:233], v189 offset:53248
	ds_read_b128 v[234:237], v189 offset:54272
	ds_read_b128 v[238:241], v189 offset:55296
	ds_read_b128 v[242:245], v189 offset:56320
	s_add_u32 s84, s48, 0x80
	s_addc_u32 s85, s49, 0
	global_load_lds_dwordx4 v130, s[84:85]
	s_add_i32 m0, s69, 0x2000
	s_add_u32 s48, s48, 0x80080
	s_addc_u32 s49, s49, 0
	s_add_i32 s69, s70, s23
	s_add_u32 s84, s48, 0xfff80000
	s_addc_u32 s85, s49, -1
	global_load_lds_dwordx4 v134, s[84:85]
	s_mov_b32 m0, s69
	s_nop 0
	global_load_lds_dwordx4 v130, s[48:49]
	s_add_i32 m0, s69, 0x2000
	s_nop 0
	global_load_lds_dwordx4 v134, s[48:49]
	s_mov_b32 m0, s18
	s_nop 0
	s_add_u32 s84, s82, 0xfff80080
	s_addc_u32 s85, s83, -1
	global_load_lds_dwordx4 v128, s[84:85]
	s_mov_b32 m0, s72
	s_nop 0
	s_add_u32 s84, s82, 0xfff80080
	s_addc_u32 s85, s83, -1
	global_load_lds_dwordx4 v132, s[84:85]
	s_waitcnt vmcnt(8)
	s_waitcnt lgkmcnt(0)
	s_barrier
	s_setprio 1
	s_waitcnt lgkmcnt(0)
	v_mfma_f32_16x16x32_bf16 v[60:63], v[144:147], v[214:217], v[60:63]
	v_mfma_f32_16x16x32_bf16 v[56:59], v[152:155], v[214:217], v[56:59]
	v_mfma_f32_16x16x32_bf16 v[44:47], v[144:147], v[222:225], v[44:47]
	v_mfma_f32_16x16x32_bf16 v[40:43], v[152:155], v[222:225], v[40:43]
	v_mfma_f32_16x16x32_bf16 v[28:31], v[144:147], v[230:233], v[28:31]
	v_mfma_f32_16x16x32_bf16 v[24:27], v[152:155], v[230:233], v[24:27]
	v_mfma_f32_16x16x32_bf16 v[12:15], v[144:147], v[238:241], v[12:15]
	v_mfma_f32_16x16x32_bf16 v[8:11], v[152:155], v[238:241], v[8:11]
	v_mfma_f32_16x16x32_bf16 v[60:63], v[148:151], v[218:221], v[60:63]
	v_mfma_f32_16x16x32_bf16 v[56:59], v[156:159], v[218:221], v[56:59]
	v_mfma_f32_16x16x32_bf16 v[44:47], v[148:151], v[226:229], v[44:47]
	v_mfma_f32_16x16x32_bf16 v[40:43], v[156:159], v[226:229], v[40:43]
	v_mfma_f32_16x16x32_bf16 v[28:31], v[148:151], v[234:237], v[28:31]
	v_mfma_f32_16x16x32_bf16 v[24:27], v[156:159], v[234:237], v[24:27]
	v_mfma_f32_16x16x32_bf16 v[12:15], v[148:151], v[242:245], v[12:15]
	v_mfma_f32_16x16x32_bf16 v[8:11], v[156:159], v[242:245], v[8:11]
	v_mfma_f32_16x16x32_bf16 v[52:55], v[160:163], v[214:217], v[52:55]
	v_mfma_f32_16x16x32_bf16 v[48:51], v[206:209], v[214:217], v[48:51]
	v_mfma_f32_16x16x32_bf16 v[36:39], v[160:163], v[222:225], v[36:39]
	v_mfma_f32_16x16x32_bf16 v[32:35], v[206:209], v[222:225], v[32:35]
	v_mfma_f32_16x16x32_bf16 v[20:23], v[160:163], v[230:233], v[20:23]
	v_mfma_f32_16x16x32_bf16 v[16:19], v[206:209], v[230:233], v[16:19]
	v_mfma_f32_16x16x32_bf16 v[4:7], v[160:163], v[238:241], v[4:7]
	v_mfma_f32_16x16x32_bf16 v[0:3], v[206:209], v[238:241], v[0:3]
	v_mfma_f32_16x16x32_bf16 v[52:55], v[164:167], v[218:221], v[52:55]
	v_mfma_f32_16x16x32_bf16 v[48:51], v[210:213], v[218:221], v[48:51]
	v_mfma_f32_16x16x32_bf16 v[36:39], v[164:167], v[226:229], v[36:39]
	v_mfma_f32_16x16x32_bf16 v[32:35], v[210:213], v[226:229], v[32:35]
	v_mfma_f32_16x16x32_bf16 v[20:23], v[164:167], v[234:237], v[20:23]
	v_mfma_f32_16x16x32_bf16 v[16:19], v[210:213], v[234:237], v[16:19]
	v_mfma_f32_16x16x32_bf16 v[4:7], v[164:167], v[242:245], v[4:7]
	v_mfma_f32_16x16x32_bf16 v[0:3], v[210:213], v[242:245], v[0:3]
	s_setprio 0
	s_barrier
	s_add_i32 s67, s67, 2
	s_add_u32 s46, s46, 0x100
	s_addc_u32 s47, s47, 0
	s_add_u32 s14, s14, 0x100
	s_addc_u32 s15, s15, 0
	s_cmp_gt_u32 s67, 29
	s_cbranch_scc0 .LBB0_823
	s_and_b64 vcc, exec, s[64:65]
	s_cbranch_vccz .LBB0_826
	s_barrier

.LBB0_2001:
	s_add_u32 s5, s48, 0xfff80080
	s_addc_u32 s10, s49, -1
	s_add_i32 s31, 0, 0x10000
	s_cmp_eq_u32 s29, 28
	s_cselect_b32 s53, s45, s10
	s_cselect_b32 s52, s44, s5
	v_add_u32_e32 v144, s31, v146
	s_cselect_b32 s51, s47, s15
	s_cselect_b32 s50, s46, s14
	s_add_i32 s5, 0, 0x14000
	ds_read_b128 v[140:143], v144
	ds_read_b128 v[150:153], v144 offset:1024
	ds_read_b128 v[154:157], v144 offset:2048
	ds_read_b128 v[158:161], v144 offset:3072
	v_add_u32_e32 v144, s5, v146
	ds_read_b128 v[162:165], v144
	ds_read_b128 v[166:169], v144 offset:1024
	ds_read_b128 v[170:173], v144 offset:2048
	ds_read_b128 v[182:185], v144 offset:3072
	s_add_i32 m0, s59, 0xc000
	ds_read_b128 v[186:189], v149
	ds_read_b128 v[206:209], v149 offset:1024
	ds_read_b128 v[210:213], v149 offset:2048
	ds_read_b128 v[214:217], v149 offset:3072
	ds_read_b128 v[218:221], v149 offset:4096
	ds_read_b128 v[222:225], v149 offset:5120
	ds_read_b128 v[226:229], v149 offset:6144
	ds_read_b128 v[230:233], v149 offset:7168
	global_load_lds_dwordx4 v136, s[48:49]
	s_add_i32 m0, s59, 0xe000
	s_nop 0
	global_load_lds_dwordx4 v138, s[48:49]
	s_waitcnt vmcnt(8)
	s_waitcnt lgkmcnt(0)
	s_barrier
	s_setprio 1
	s_waitcnt lgkmcnt(0)
	v_mfma_f32_16x16x32_bf16 v[124:127], v[140:143], v[186:189], v[124:127]
	v_mfma_f32_16x16x32_bf16 v[120:123], v[154:157], v[186:189], v[120:123]
	v_mfma_f32_16x16x32_bf16 v[108:111], v[140:143], v[210:213], v[108:111]
	v_mfma_f32_16x16x32_bf16 v[104:107], v[154:157], v[210:213], v[104:107]
	v_mfma_f32_16x16x32_bf16 v[92:95], v[140:143], v[218:221], v[92:95]
	v_mfma_f32_16x16x32_bf16 v[88:91], v[154:157], v[218:221], v[88:91]
	v_mfma_f32_16x16x32_bf16 v[76:79], v[140:143], v[226:229], v[76:79]
	v_mfma_f32_16x16x32_bf16 v[72:75], v[154:157], v[226:229], v[72:75]
	v_mfma_f32_16x16x32_bf16 v[124:127], v[150:153], v[206:209], v[124:127]
	v_mfma_f32_16x16x32_bf16 v[120:123], v[158:161], v[206:209], v[120:123]
	v_mfma_f32_16x16x32_bf16 v[108:111], v[150:153], v[214:217], v[108:111]
	v_mfma_f32_16x16x32_bf16 v[104:107], v[158:161], v[214:217], v[104:107]
	v_mfma_f32_16x16x32_bf16 v[92:95], v[150:153], v[222:225], v[92:95]
	v_mfma_f32_16x16x32_bf16 v[88:91], v[158:161], v[222:225], v[88:91]
	v_mfma_f32_16x16x32_bf16 v[76:79], v[150:153], v[230:233], v[76:79]
	v_mfma_f32_16x16x32_bf16 v[72:75], v[158:161], v[230:233], v[72:75]
	v_mfma_f32_16x16x32_bf16 v[116:119], v[162:165], v[186:189], v[116:119]
	v_mfma_f32_16x16x32_bf16 v[112:115], v[170:173], v[186:189], v[112:115]
	v_mfma_f32_16x16x32_bf16 v[100:103], v[162:165], v[210:213], v[100:103]
	v_mfma_f32_16x16x32_bf16 v[96:99], v[170:173], v[210:213], v[96:99]
	v_mfma_f32_16x16x32_bf16 v[84:87], v[162:165], v[218:221], v[84:87]
	v_mfma_f32_16x16x32_bf16 v[80:83], v[170:173], v[218:221], v[80:83]
	v_mfma_f32_16x16x32_bf16 v[68:71], v[162:165], v[226:229], v[68:71]
	v_mfma_f32_16x16x32_bf16 v[64:67], v[170:173], v[226:229], v[64:67]
	v_mfma_f32_16x16x32_bf16 v[116:119], v[166:169], v[206:209], v[116:119]
	v_mfma_f32_16x16x32_bf16 v[112:115], v[182:185], v[206:209], v[112:115]
	v_mfma_f32_16x16x32_bf16 v[100:103], v[166:169], v[214:217], v[100:103]
	v_mfma_f32_16x16x32_bf16 v[96:99], v[182:185], v[214:217], v[96:99]
	v_mfma_f32_16x16x32_bf16 v[84:87], v[166:169], v[222:225], v[84:87]
	v_mfma_f32_16x16x32_bf16 v[80:83], v[182:185], v[222:225], v[80:83]
	v_mfma_f32_16x16x32_bf16 v[68:71], v[166:169], v[230:233], v[68:71]
	v_mfma_f32_16x16x32_bf16 v[64:67], v[182:185], v[230:233], v[64:67]
	s_setprio 0
	s_barrier
	s_add_i32 s10, s31, s58
	s_mov_b32 m0, s10
	ds_read_b128 v[186:189], v149 offset:16384
	ds_read_b128 v[206:209], v149 offset:17408
	ds_read_b128 v[210:213], v149 offset:18432
	ds_read_b128 v[214:217], v149 offset:19456
	ds_read_b128 v[218:221], v149 offset:20480
	ds_read_b128 v[222:225], v149 offset:21504
	ds_read_b128 v[226:229], v149 offset:22528
	ds_read_b128 v[230:233], v149 offset:23552
	global_load_lds_dwordx4 v176, s[50:51]
	s_add_i32 m0, s10, 0x2000
	s_add_u32 s74, s50, 0x80000
	s_addc_u32 s75, s51, 0
	s_add_i32 s5, s5, s58
	global_load_lds_dwordx4 v132, s[50:51]
	s_mov_b32 m0, s5
	s_nop 0
	global_load_lds_dwordx4 v176, s[74:75]
	s_add_i32 m0, s5, 0x2000
	s_nop 0
	global_load_lds_dwordx4 v132, s[74:75]
	s_mov_b32 m0, s59
	s_nop 0
	global_load_lds_dwordx4 v128, s[52:53]
	s_mov_b32 m0, s60
	s_nop 0
	global_load_lds_dwordx4 v130, s[52:53]
	s_waitcnt vmcnt(8)
	s_waitcnt lgkmcnt(0)
	s_barrier
	s_setprio 1
	s_waitcnt lgkmcnt(0)
	v_mfma_f32_16x16x32_bf16 v[60:63], v[140:143], v[186:189], v[60:63]
	v_mfma_f32_16x16x32_bf16 v[56:59], v[154:157], v[186:189], v[56:59]
	v_mfma_f32_16x16x32_bf16 v[44:47], v[140:143], v[210:213], v[44:47]
	v_mfma_f32_16x16x32_bf16 v[40:43], v[154:157], v[210:213], v[40:43]
	v_mfma_f32_16x16x32_bf16 v[28:31], v[140:143], v[218:221], v[28:31]
	v_mfma_f32_16x16x32_bf16 v[24:27], v[154:157], v[218:221], v[24:27]
	v_mfma_f32_16x16x32_bf16 v[12:15], v[140:143], v[226:229], v[12:15]
	v_mfma_f32_16x16x32_bf16 v[8:11], v[154:157], v[226:229], v[8:11]
	v_mfma_f32_16x16x32_bf16 v[60:63], v[150:153], v[206:209], v[60:63]
	v_mfma_f32_16x16x32_bf16 v[56:59], v[158:161], v[206:209], v[56:59]
	v_mfma_f32_16x16x32_bf16 v[44:47], v[150:153], v[214:217], v[44:47]
	v_mfma_f32_16x16x32_bf16 v[40:43], v[158:161], v[214:217], v[40:43]
	v_mfma_f32_16x16x32_bf16 v[28:31], v[150:153], v[222:225], v[28:31]
	v_mfma_f32_16x16x32_bf16 v[24:27], v[158:161], v[222:225], v[24:27]
	v_mfma_f32_16x16x32_bf16 v[12:15], v[150:153], v[230:233], v[12:15]
	v_mfma_f32_16x16x32_bf16 v[8:11], v[158:161], v[230:233], v[8:11]
	v_mfma_f32_16x16x32_bf16 v[52:55], v[162:165], v[186:189], v[52:55]
	v_mfma_f32_16x16x32_bf16 v[48:51], v[170:173], v[186:189], v[48:51]
	v_mfma_f32_16x16x32_bf16 v[36:39], v[162:165], v[210:213], v[36:39]
	v_mfma_f32_16x16x32_bf16 v[32:35], v[170:173], v[210:213], v[32:35]
	v_mfma_f32_16x16x32_bf16 v[20:23], v[162:165], v[218:221], v[20:23]
	v_mfma_f32_16x16x32_bf16 v[16:19], v[170:173], v[218:221], v[16:19]
	v_mfma_f32_16x16x32_bf16 v[4:7], v[162:165], v[226:229], v[4:7]
	v_mfma_f32_16x16x32_bf16 v[0:3], v[170:173], v[226:229], v[0:3]
	v_mfma_f32_16x16x32_bf16 v[52:55], v[166:169], v[206:209], v[52:55]
	v_mfma_f32_16x16x32_bf16 v[48:51], v[182:185], v[206:209], v[48:51]
	v_mfma_f32_16x16x32_bf16 v[36:39], v[166:169], v[214:217], v[36:39]
	v_mfma_f32_16x16x32_bf16 v[32:35], v[182:185], v[214:217], v[32:35]
	v_mfma_f32_16x16x32_bf16 v[20:23], v[166:169], v[222:225], v[20:23]
	v_mfma_f32_16x16x32_bf16 v[16:19], v[182:185], v[222:225], v[16:19]
	v_mfma_f32_16x16x32_bf16 v[4:7], v[166:169], v[230:233], v[4:7]
	v_mfma_f32_16x16x32_bf16 v[0:3], v[182:185], v[230:233], v[0:3]
	s_setprio 0
	s_barrier
	s_add_i32 s5, 0, 0x18000
	s_add_i32 s10, 0, 0x1c000
	v_add_u32_e32 v158, s5, v146
	v_add_u32_e32 v178, s10, v146
	ds_read_b128 v[140:143], v158
	ds_read_b128 v[150:153], v158 offset:1024
	ds_read_b128 v[154:157], v158 offset:2048
	ds_read_b128 v[158:161], v158 offset:3072
	ds_read_b128 v[162:165], v178
	ds_read_b128 v[166:169], v178 offset:1024
	ds_read_b128 v[170:173], v178 offset:2048
	ds_read_b128 v[182:185], v178 offset:3072
	s_add_u32 s52, s52, 0x80000
	s_addc_u32 s53, s53, 0
	s_mov_b32 m0, s61
	ds_read_b128 v[186:189], v149 offset:32768
	ds_read_b128 v[206:209], v149 offset:33792
	ds_read_b128 v[210:213], v149 offset:34816
	ds_read_b128 v[214:217], v149 offset:35840
	ds_read_b128 v[218:221], v149 offset:36864
	ds_read_b128 v[222:225], v149 offset:37888
	ds_read_b128 v[226:229], v149 offset:38912
	ds_read_b128 v[230:233], v149 offset:39936
	global_load_lds_dwordx4 v128, s[52:53]
	s_mov_b32 m0, s62
	s_nop 0
	global_load_lds_dwordx4 v130, s[52:53]
	s_waitcnt vmcnt(8)
	s_waitcnt lgkmcnt(0)
	s_barrier
	s_setprio 1
	s_waitcnt lgkmcnt(0)
	v_mfma_f32_16x16x32_bf16 v[124:127], v[140:143], v[186:189], v[124:127]
	v_mfma_f32_16x16x32_bf16 v[120:123], v[154:157], v[186:189], v[120:123]
	v_mfma_f32_16x16x32_bf16 v[108:111], v[140:143], v[210:213], v[108:111]
	v_mfma_f32_16x16x32_bf16 v[104:107], v[154:157], v[210:213], v[104:107]
	v_mfma_f32_16x16x32_bf16 v[92:95], v[140:143], v[218:221], v[92:95]
	v_mfma_f32_16x16x32_bf16 v[88:91], v[154:157], v[218:221], v[88:91]
	v_mfma_f32_16x16x32_bf16 v[76:79], v[140:143], v[226:229], v[76:79]
	v_mfma_f32_16x16x32_bf16 v[72:75], v[154:157], v[226:229], v[72:75]
	v_mfma_f32_16x16x32_bf16 v[124:127], v[150:153], v[206:209], v[124:127]
	v_mfma_f32_16x16x32_bf16 v[120:123], v[158:161], v[206:209], v[120:123]
	v_mfma_f32_16x16x32_bf16 v[108:111], v[150:153], v[214:217], v[108:111]
	v_mfma_f32_16x16x32_bf16 v[104:107], v[158:161], v[214:217], v[104:107]
	v_mfma_f32_16x16x32_bf16 v[92:95], v[150:153], v[222:225], v[92:95]
	v_mfma_f32_16x16x32_bf16 v[88:91], v[158:161], v[222:225], v[88:91]
	v_mfma_f32_16x16x32_bf16 v[76:79], v[150:153], v[230:233], v[76:79]
	v_mfma_f32_16x16x32_bf16 v[72:75], v[158:161], v[230:233], v[72:75]
	v_mfma_f32_16x16x32_bf16 v[116:119], v[162:165], v[186:189], v[116:119]
	v_mfma_f32_16x16x32_bf16 v[112:115], v[170:173], v[186:189], v[112:115]
	v_mfma_f32_16x16x32_bf16 v[100:103], v[162:165], v[210:213], v[100:103]
	v_mfma_f32_16x16x32_bf16 v[96:99], v[170:173], v[210:213], v[96:99]
	v_mfma_f32_16x16x32_bf16 v[84:87], v[162:165], v[218:221], v[84:87]
	v_mfma_f32_16x16x32_bf16 v[80:83], v[170:173], v[218:221], v[80:83]
	v_mfma_f32_16x16x32_bf16 v[68:71], v[162:165], v[226:229], v[68:71]
	v_mfma_f32_16x16x32_bf16 v[64:67], v[170:173], v[226:229], v[64:67]
	v_mfma_f32_16x16x32_bf16 v[116:119], v[166:169], v[206:209], v[116:119]
	v_mfma_f32_16x16x32_bf16 v[112:115], v[182:185], v[206:209], v[112:115]
	v_mfma_f32_16x16x32_bf16 v[100:103], v[166:169], v[214:217], v[100:103]
	v_mfma_f32_16x16x32_bf16 v[96:99], v[182:185], v[214:217], v[96:99]
	v_mfma_f32_16x16x32_bf16 v[84:87], v[166:169], v[222:225], v[84:87]
	v_mfma_f32_16x16x32_bf16 v[80:83], v[182:185], v[222:225], v[80:83]
	v_mfma_f32_16x16x32_bf16 v[68:71], v[166:169], v[230:233], v[68:71]
	v_mfma_f32_16x16x32_bf16 v[64:67], v[182:185], v[230:233], v[64:67]
	s_setprio 0
	s_barrier
	s_add_i32 s5, s5, s58
	s_mov_b32 m0, s5
	ds_read_b128 v[186:189], v149 offset:49152
	ds_read_b128 v[206:209], v149 offset:50176
	ds_read_b128 v[210:213], v149 offset:51200
	ds_read_b128 v[214:217], v149 offset:52224
	ds_read_b128 v[218:221], v149 offset:53248
	ds_read_b128 v[222:225], v149 offset:54272
	ds_read_b128 v[226:229], v149 offset:55296
	ds_read_b128 v[230:233], v149 offset:56320
	s_add_u32 s74, s50, 0x80
	s_addc_u32 s75, s51, 0
	global_load_lds_dwordx4 v176, s[74:75]
	s_add_i32 m0, s5, 0x2000
	s_add_u32 s50, s50, 0x80080
	s_addc_u32 s51, s51, 0
	s_add_i32 s5, s10, s58
	s_add_u32 s74, s50, 0xfff80000
	s_addc_u32 s75, s51, -1
	global_load_lds_dwordx4 v132, s[74:75]
	s_mov_b32 m0, s5
	s_nop 0
	global_load_lds_dwordx4 v176, s[50:51]
	s_add_i32 m0, s5, 0x2000
	s_nop 0
	global_load_lds_dwordx4 v132, s[50:51]
	s_mov_b32 m0, s64
	s_nop 0
	s_add_u32 s74, s52, 0xfff80080
	s_addc_u32 s75, s53, -1
	global_load_lds_dwordx4 v128, s[74:75]
	s_mov_b32 m0, s65
	s_nop 0
	s_add_u32 s74, s52, 0xfff80080
	s_addc_u32 s75, s53, -1
	global_load_lds_dwordx4 v130, s[74:75]
	s_waitcnt vmcnt(8)
	s_waitcnt lgkmcnt(0)
	s_barrier
	s_setprio 1
	s_waitcnt lgkmcnt(0)
	v_mfma_f32_16x16x32_bf16 v[60:63], v[140:143], v[186:189], v[60:63]
	v_mfma_f32_16x16x32_bf16 v[56:59], v[154:157], v[186:189], v[56:59]
	v_mfma_f32_16x16x32_bf16 v[44:47], v[140:143], v[210:213], v[44:47]
	v_mfma_f32_16x16x32_bf16 v[40:43], v[154:157], v[210:213], v[40:43]
	v_mfma_f32_16x16x32_bf16 v[28:31], v[140:143], v[218:221], v[28:31]
	v_mfma_f32_16x16x32_bf16 v[24:27], v[154:157], v[218:221], v[24:27]
	v_mfma_f32_16x16x32_bf16 v[12:15], v[140:143], v[226:229], v[12:15]
	v_mfma_f32_16x16x32_bf16 v[8:11], v[154:157], v[226:229], v[8:11]
	v_mfma_f32_16x16x32_bf16 v[60:63], v[150:153], v[206:209], v[60:63]
	v_mfma_f32_16x16x32_bf16 v[56:59], v[158:161], v[206:209], v[56:59]
	v_mfma_f32_16x16x32_bf16 v[44:47], v[150:153], v[214:217], v[44:47]
	v_mfma_f32_16x16x32_bf16 v[40:43], v[158:161], v[214:217], v[40:43]
	v_mfma_f32_16x16x32_bf16 v[28:31], v[150:153], v[222:225], v[28:31]
	v_mfma_f32_16x16x32_bf16 v[24:27], v[158:161], v[222:225], v[24:27]
	v_mfma_f32_16x16x32_bf16 v[12:15], v[150:153], v[230:233], v[12:15]
	v_mfma_f32_16x16x32_bf16 v[8:11], v[158:161], v[230:233], v[8:11]
	v_mfma_f32_16x16x32_bf16 v[52:55], v[162:165], v[186:189], v[52:55]
	v_mfma_f32_16x16x32_bf16 v[48:51], v[170:173], v[186:189], v[48:51]
	v_mfma_f32_16x16x32_bf16 v[36:39], v[162:165], v[210:213], v[36:39]
	v_mfma_f32_16x16x32_bf16 v[32:35], v[170:173], v[210:213], v[32:35]
	v_mfma_f32_16x16x32_bf16 v[20:23], v[162:165], v[218:221], v[20:23]
	v_mfma_f32_16x16x32_bf16 v[16:19], v[170:173], v[218:221], v[16:19]
	v_mfma_f32_16x16x32_bf16 v[4:7], v[162:165], v[226:229], v[4:7]
	v_mfma_f32_16x16x32_bf16 v[0:3], v[170:173], v[226:229], v[0:3]
	v_mfma_f32_16x16x32_bf16 v[52:55], v[166:169], v[206:209], v[52:55]
	v_mfma_f32_16x16x32_bf16 v[48:51], v[182:185], v[206:209], v[48:51]
	v_mfma_f32_16x16x32_bf16 v[36:39], v[166:169], v[214:217], v[36:39]
	v_mfma_f32_16x16x32_bf16 v[32:35], v[182:185], v[214:217], v[32:35]
	v_mfma_f32_16x16x32_bf16 v[20:23], v[166:169], v[222:225], v[20:23]
	v_mfma_f32_16x16x32_bf16 v[16:19], v[182:185], v[222:225], v[16:19]
	v_mfma_f32_16x16x32_bf16 v[4:7], v[166:169], v[230:233], v[4:7]
	v_mfma_f32_16x16x32_bf16 v[0:3], v[182:185], v[230:233], v[0:3]
	s_setprio 0
	s_barrier
	s_add_i32 s29, s29, 2
	s_add_u32 s48, s48, 0x100
	s_addc_u32 s49, s49, 0
	s_add_u32 s14, s14, 0x100
	s_addc_u32 s15, s15, 0
	s_cmp_gt_u32 s29, 29
	s_cbranch_scc0 .LBB0_2001
	s_and_b64 vcc, exec, s[26:27]
	s_cbranch_vccz .LBB0_2004
	s_barrier

.LBB0_2084:
	s_add_u32 s5, s50, 0xfff80080
	s_addc_u32 s10, s51, -1
	s_add_i32 s29, 0, 0x10000
	s_cmp_eq_u32 s27, 28
	s_cselect_b32 s55, s47, s10
	s_cselect_b32 s54, s46, s5
	v_add_u32_e32 v154, s29, v157
	s_cselect_b32 s53, s49, s15
	s_cselect_b32 s52, s48, s14
	s_add_i32 s5, 0, 0x14000
	ds_read_b128 v[142:145], v154
	ds_read_b128 v[146:149], v154 offset:1024
	ds_read_b128 v[150:153], v154 offset:2048
	ds_read_b128 v[188:191], v154 offset:3072
	v_add_u32_e32 v154, s5, v157
	ds_read_b128 v[206:209], v154
	ds_read_b128 v[210:213], v154 offset:1024
	ds_read_b128 v[214:217], v154 offset:2048
	ds_read_b128 v[218:221], v154 offset:3072
	s_add_i32 m0, s60, 0xc000
	ds_read_b128 v[222:225], v186
	ds_read_b128 v[226:229], v186 offset:1024
	ds_read_b128 v[230:233], v186 offset:2048
	ds_read_b128 v[234:237], v186 offset:3072
	ds_read_b128 v[238:241], v186 offset:4096
	ds_read_b128 v[242:245], v186 offset:5120
	ds_read_b128 v[246:249], v186 offset:6144
	ds_read_b128 v[250:253], v186 offset:7168
	global_load_lds_dwordx4 v138, s[50:51]
	s_add_i32 m0, s60, 0xe000
	s_nop 0
	global_load_lds_dwordx4 v140, s[50:51]
	s_waitcnt vmcnt(8)
	s_waitcnt lgkmcnt(0)
	s_barrier
	s_setprio 1
	s_waitcnt lgkmcnt(0)
	v_mfma_f32_16x16x32_bf16 v[124:127], v[142:145], v[222:225], v[124:127]
	v_mfma_f32_16x16x32_bf16 v[120:123], v[150:153], v[222:225], v[120:123]
	v_mfma_f32_16x16x32_bf16 v[108:111], v[142:145], v[230:233], v[108:111]
	v_mfma_f32_16x16x32_bf16 v[104:107], v[150:153], v[230:233], v[104:107]
	v_mfma_f32_16x16x32_bf16 v[92:95], v[142:145], v[238:241], v[92:95]
	v_mfma_f32_16x16x32_bf16 v[88:91], v[150:153], v[238:241], v[88:91]
	v_mfma_f32_16x16x32_bf16 v[76:79], v[142:145], v[246:249], v[76:79]
	v_mfma_f32_16x16x32_bf16 v[72:75], v[150:153], v[246:249], v[72:75]
	v_mfma_f32_16x16x32_bf16 v[124:127], v[146:149], v[226:229], v[124:127]
	v_mfma_f32_16x16x32_bf16 v[120:123], v[188:191], v[226:229], v[120:123]
	v_mfma_f32_16x16x32_bf16 v[108:111], v[146:149], v[234:237], v[108:111]
	v_mfma_f32_16x16x32_bf16 v[104:107], v[188:191], v[234:237], v[104:107]
	v_mfma_f32_16x16x32_bf16 v[92:95], v[146:149], v[242:245], v[92:95]
	v_mfma_f32_16x16x32_bf16 v[88:91], v[188:191], v[242:245], v[88:91]
	v_mfma_f32_16x16x32_bf16 v[76:79], v[146:149], v[250:253], v[76:79]
	v_mfma_f32_16x16x32_bf16 v[72:75], v[188:191], v[250:253], v[72:75]
	v_mfma_f32_16x16x32_bf16 v[116:119], v[206:209], v[222:225], v[116:119]
	v_mfma_f32_16x16x32_bf16 v[112:115], v[214:217], v[222:225], v[112:115]
	v_mfma_f32_16x16x32_bf16 v[100:103], v[206:209], v[230:233], v[100:103]
	v_mfma_f32_16x16x32_bf16 v[96:99], v[214:217], v[230:233], v[96:99]
	v_mfma_f32_16x16x32_bf16 v[84:87], v[206:209], v[238:241], v[84:87]
	v_mfma_f32_16x16x32_bf16 v[80:83], v[214:217], v[238:241], v[80:83]
	v_mfma_f32_16x16x32_bf16 v[68:71], v[206:209], v[246:249], v[68:71]
	v_mfma_f32_16x16x32_bf16 v[64:67], v[214:217], v[246:249], v[64:67]
	v_mfma_f32_16x16x32_bf16 v[116:119], v[210:213], v[226:229], v[116:119]
	v_mfma_f32_16x16x32_bf16 v[112:115], v[218:221], v[226:229], v[112:115]
	v_mfma_f32_16x16x32_bf16 v[100:103], v[210:213], v[234:237], v[100:103]
	v_mfma_f32_16x16x32_bf16 v[96:99], v[218:221], v[234:237], v[96:99]
	v_mfma_f32_16x16x32_bf16 v[84:87], v[210:213], v[242:245], v[84:87]
	v_mfma_f32_16x16x32_bf16 v[80:83], v[218:221], v[242:245], v[80:83]
	v_mfma_f32_16x16x32_bf16 v[68:71], v[210:213], v[250:253], v[68:71]
	v_mfma_f32_16x16x32_bf16 v[64:67], v[218:221], v[250:253], v[64:67]
	s_setprio 0
	s_barrier
	s_add_i32 s10, s29, s45
	s_mov_b32 m0, s10
	ds_read_b128 v[222:225], v186 offset:16384
	ds_read_b128 v[226:229], v186 offset:17408
	ds_read_b128 v[230:233], v186 offset:18432
	ds_read_b128 v[234:237], v186 offset:19456
	ds_read_b128 v[238:241], v186 offset:20480
	ds_read_b128 v[242:245], v186 offset:21504
	ds_read_b128 v[246:249], v186 offset:22528
	ds_read_b128 v[250:253], v186 offset:23552
	global_load_lds_dwordx4 v130, s[52:53]
	s_add_i32 m0, s10, 0x2000
	s_add_u32 s74, s52, 0x80000
	s_addc_u32 s75, s53, 0
	s_add_i32 s5, s5, s45
	global_load_lds_dwordx4 v134, s[52:53]
	s_mov_b32 m0, s5
	s_nop 0
	global_load_lds_dwordx4 v130, s[74:75]
	s_add_i32 m0, s5, 0x2000
	s_nop 0
	global_load_lds_dwordx4 v134, s[74:75]
	s_mov_b32 m0, s60
	s_nop 0
	global_load_lds_dwordx4 v128, s[54:55]
	s_mov_b32 m0, s61
	s_nop 0
	global_load_lds_dwordx4 v132, s[54:55]
	s_waitcnt vmcnt(8)
	s_waitcnt lgkmcnt(0)
	s_barrier
	s_setprio 1
	s_waitcnt lgkmcnt(0)
	v_mfma_f32_16x16x32_bf16 v[60:63], v[142:145], v[222:225], v[60:63]
	v_mfma_f32_16x16x32_bf16 v[56:59], v[150:153], v[222:225], v[56:59]
	v_mfma_f32_16x16x32_bf16 v[44:47], v[142:145], v[230:233], v[44:47]
	v_mfma_f32_16x16x32_bf16 v[40:43], v[150:153], v[230:233], v[40:43]
	v_mfma_f32_16x16x32_bf16 v[28:31], v[142:145], v[238:241], v[28:31]
	v_mfma_f32_16x16x32_bf16 v[24:27], v[150:153], v[238:241], v[24:27]
	v_mfma_f32_16x16x32_bf16 v[12:15], v[142:145], v[246:249], v[12:15]
	v_mfma_f32_16x16x32_bf16 v[8:11], v[150:153], v[246:249], v[8:11]
	v_mfma_f32_16x16x32_bf16 v[60:63], v[146:149], v[226:229], v[60:63]
	v_mfma_f32_16x16x32_bf16 v[56:59], v[188:191], v[226:229], v[56:59]
	v_mfma_f32_16x16x32_bf16 v[44:47], v[146:149], v[234:237], v[44:47]
	v_mfma_f32_16x16x32_bf16 v[40:43], v[188:191], v[234:237], v[40:43]
	v_mfma_f32_16x16x32_bf16 v[28:31], v[146:149], v[242:245], v[28:31]
	v_mfma_f32_16x16x32_bf16 v[24:27], v[188:191], v[242:245], v[24:27]
	v_mfma_f32_16x16x32_bf16 v[12:15], v[146:149], v[250:253], v[12:15]
	v_mfma_f32_16x16x32_bf16 v[8:11], v[188:191], v[250:253], v[8:11]
	v_mfma_f32_16x16x32_bf16 v[52:55], v[206:209], v[222:225], v[52:55]
	v_mfma_f32_16x16x32_bf16 v[48:51], v[214:217], v[222:225], v[48:51]
	v_mfma_f32_16x16x32_bf16 v[36:39], v[206:209], v[230:233], v[36:39]
	v_mfma_f32_16x16x32_bf16 v[32:35], v[214:217], v[230:233], v[32:35]
	v_mfma_f32_16x16x32_bf16 v[20:23], v[206:209], v[238:241], v[20:23]
	v_mfma_f32_16x16x32_bf16 v[16:19], v[214:217], v[238:241], v[16:19]
	v_mfma_f32_16x16x32_bf16 v[4:7], v[206:209], v[246:249], v[4:7]
	v_mfma_f32_16x16x32_bf16 v[0:3], v[214:217], v[246:249], v[0:3]
	v_mfma_f32_16x16x32_bf16 v[52:55], v[210:213], v[226:229], v[52:55]
	v_mfma_f32_16x16x32_bf16 v[48:51], v[218:221], v[226:229], v[48:51]
	v_mfma_f32_16x16x32_bf16 v[36:39], v[210:213], v[234:237], v[36:39]
	v_mfma_f32_16x16x32_bf16 v[32:35], v[218:221], v[234:237], v[32:35]
	v_mfma_f32_16x16x32_bf16 v[20:23], v[210:213], v[242:245], v[20:23]
	v_mfma_f32_16x16x32_bf16 v[16:19], v[218:221], v[242:245], v[16:19]
	v_mfma_f32_16x16x32_bf16 v[4:7], v[210:213], v[250:253], v[4:7]
	v_mfma_f32_16x16x32_bf16 v[0:3], v[218:221], v[250:253], v[0:3]
	s_setprio 0
	s_barrier
	s_add_i32 s5, 0, 0x18000
	v_add_u32_e32 v187, s5, v157
	s_add_i32 s10, 0, 0x1c000
	ds_read_b128 v[142:145], v187
	ds_read_b128 v[146:149], v187 offset:1024
	ds_read_b128 v[150:153], v187 offset:2048
	ds_read_b128 v[188:191], v187 offset:3072
	v_add_u32_e32 v187, s10, v157
	ds_read_b128 v[206:209], v187
	ds_read_b128 v[210:213], v187 offset:1024
	ds_read_b128 v[214:217], v187 offset:2048
	ds_read_b128 v[218:221], v187 offset:3072
	s_add_u32 s54, s54, 0x80000
	s_addc_u32 s55, s55, 0
	s_mov_b32 m0, s62
	ds_read_b128 v[222:225], v186 offset:32768
	ds_read_b128 v[226:229], v186 offset:33792
	ds_read_b128 v[230:233], v186 offset:34816
	ds_read_b128 v[234:237], v186 offset:35840
	ds_read_b128 v[238:241], v186 offset:36864
	ds_read_b128 v[242:245], v186 offset:37888
	ds_read_b128 v[246:249], v186 offset:38912
	ds_read_b128 v[250:253], v186 offset:39936
	global_load_lds_dwordx4 v128, s[54:55]
	s_mov_b32 m0, s63
	s_nop 0
	global_load_lds_dwordx4 v132, s[54:55]
	s_waitcnt vmcnt(8)
	s_waitcnt lgkmcnt(0)
	s_barrier
	s_setprio 1
	s_waitcnt lgkmcnt(0)
	v_mfma_f32_16x16x32_bf16 v[124:127], v[142:145], v[222:225], v[124:127]
	v_mfma_f32_16x16x32_bf16 v[120:123], v[150:153], v[222:225], v[120:123]
	v_mfma_f32_16x16x32_bf16 v[108:111], v[142:145], v[230:233], v[108:111]
	v_mfma_f32_16x16x32_bf16 v[104:107], v[150:153], v[230:233], v[104:107]
	v_mfma_f32_16x16x32_bf16 v[92:95], v[142:145], v[238:241], v[92:95]
	v_mfma_f32_16x16x32_bf16 v[88:91], v[150:153], v[238:241], v[88:91]
	v_mfma_f32_16x16x32_bf16 v[76:79], v[142:145], v[246:249], v[76:79]
	v_mfma_f32_16x16x32_bf16 v[72:75], v[150:153], v[246:249], v[72:75]
	v_mfma_f32_16x16x32_bf16 v[124:127], v[146:149], v[226:229], v[124:127]
	v_mfma_f32_16x16x32_bf16 v[120:123], v[188:191], v[226:229], v[120:123]
	v_mfma_f32_16x16x32_bf16 v[108:111], v[146:149], v[234:237], v[108:111]
	v_mfma_f32_16x16x32_bf16 v[104:107], v[188:191], v[234:237], v[104:107]
	v_mfma_f32_16x16x32_bf16 v[92:95], v[146:149], v[242:245], v[92:95]
	v_mfma_f32_16x16x32_bf16 v[88:91], v[188:191], v[242:245], v[88:91]
	v_mfma_f32_16x16x32_bf16 v[76:79], v[146:149], v[250:253], v[76:79]
	v_mfma_f32_16x16x32_bf16 v[72:75], v[188:191], v[250:253], v[72:75]
	v_mfma_f32_16x16x32_bf16 v[116:119], v[206:209], v[222:225], v[116:119]
	v_mfma_f32_16x16x32_bf16 v[112:115], v[214:217], v[222:225], v[112:115]
	v_mfma_f32_16x16x32_bf16 v[100:103], v[206:209], v[230:233], v[100:103]
	v_mfma_f32_16x16x32_bf16 v[96:99], v[214:217], v[230:233], v[96:99]
	v_mfma_f32_16x16x32_bf16 v[84:87], v[206:209], v[238:241], v[84:87]
	v_mfma_f32_16x16x32_bf16 v[80:83], v[214:217], v[238:241], v[80:83]
	v_mfma_f32_16x16x32_bf16 v[68:71], v[206:209], v[246:249], v[68:71]
	v_mfma_f32_16x16x32_bf16 v[64:67], v[214:217], v[246:249], v[64:67]
	v_mfma_f32_16x16x32_bf16 v[116:119], v[210:213], v[226:229], v[116:119]
	v_mfma_f32_16x16x32_bf16 v[112:115], v[218:221], v[226:229], v[112:115]
	v_mfma_f32_16x16x32_bf16 v[100:103], v[210:213], v[234:237], v[100:103]
	v_mfma_f32_16x16x32_bf16 v[96:99], v[218:221], v[234:237], v[96:99]
	v_mfma_f32_16x16x32_bf16 v[84:87], v[210:213], v[242:245], v[84:87]
	v_mfma_f32_16x16x32_bf16 v[80:83], v[218:221], v[242:245], v[80:83]
	v_mfma_f32_16x16x32_bf16 v[68:71], v[210:213], v[250:253], v[68:71]
	v_mfma_f32_16x16x32_bf16 v[64:67], v[218:221], v[250:253], v[64:67]
	s_setprio 0
	s_barrier
	s_add_i32 s5, s5, s45
	s_mov_b32 m0, s5
	ds_read_b128 v[222:225], v186 offset:49152
	ds_read_b128 v[226:229], v186 offset:50176
	ds_read_b128 v[230:233], v186 offset:51200
	ds_read_b128 v[234:237], v186 offset:52224
	ds_read_b128 v[238:241], v186 offset:53248
	ds_read_b128 v[242:245], v186 offset:54272
	ds_read_b128 v[246:249], v186 offset:55296
	ds_read_b128 v[250:253], v186 offset:56320
	s_add_u32 s74, s52, 0x80
	s_addc_u32 s75, s53, 0
	global_load_lds_dwordx4 v130, s[74:75]
	s_add_i32 m0, s5, 0x2000
	s_add_u32 s52, s52, 0x80080
	s_addc_u32 s53, s53, 0
	s_add_i32 s5, s10, s45
	s_add_u32 s74, s52, 0xfff80000
	s_addc_u32 s75, s53, -1
	global_load_lds_dwordx4 v134, s[74:75]
	s_mov_b32 m0, s5
	s_nop 0
	global_load_lds_dwordx4 v130, s[52:53]
	s_add_i32 m0, s5, 0x2000
	s_nop 0
	global_load_lds_dwordx4 v134, s[52:53]
	s_mov_b32 m0, s64
	s_nop 0
	s_add_u32 s74, s54, 0xfff80080
	s_addc_u32 s75, s55, -1
	global_load_lds_dwordx4 v128, s[74:75]
	s_mov_b32 m0, s65
	s_nop 0
	s_add_u32 s74, s54, 0xfff80080
	s_addc_u32 s75, s55, -1
	global_load_lds_dwordx4 v132, s[74:75]
	s_waitcnt vmcnt(8)
	s_waitcnt lgkmcnt(0)
	s_barrier
	s_setprio 1
	s_waitcnt lgkmcnt(0)
	v_mfma_f32_16x16x32_bf16 v[60:63], v[142:145], v[222:225], v[60:63]
	v_mfma_f32_16x16x32_bf16 v[56:59], v[150:153], v[222:225], v[56:59]
	v_mfma_f32_16x16x32_bf16 v[44:47], v[142:145], v[230:233], v[44:47]
	v_mfma_f32_16x16x32_bf16 v[40:43], v[150:153], v[230:233], v[40:43]
	v_mfma_f32_16x16x32_bf16 v[28:31], v[142:145], v[238:241], v[28:31]
	v_mfma_f32_16x16x32_bf16 v[24:27], v[150:153], v[238:241], v[24:27]
	v_mfma_f32_16x16x32_bf16 v[12:15], v[142:145], v[246:249], v[12:15]
	v_mfma_f32_16x16x32_bf16 v[8:11], v[150:153], v[246:249], v[8:11]
	v_mfma_f32_16x16x32_bf16 v[60:63], v[146:149], v[226:229], v[60:63]
	v_mfma_f32_16x16x32_bf16 v[56:59], v[188:191], v[226:229], v[56:59]
	v_mfma_f32_16x16x32_bf16 v[44:47], v[146:149], v[234:237], v[44:47]
	v_mfma_f32_16x16x32_bf16 v[40:43], v[188:191], v[234:237], v[40:43]
	v_mfma_f32_16x16x32_bf16 v[28:31], v[146:149], v[242:245], v[28:31]
	v_mfma_f32_16x16x32_bf16 v[24:27], v[188:191], v[242:245], v[24:27]
	v_mfma_f32_16x16x32_bf16 v[12:15], v[146:149], v[250:253], v[12:15]
	v_mfma_f32_16x16x32_bf16 v[8:11], v[188:191], v[250:253], v[8:11]
	v_mfma_f32_16x16x32_bf16 v[52:55], v[206:209], v[222:225], v[52:55]
	v_mfma_f32_16x16x32_bf16 v[48:51], v[214:217], v[222:225], v[48:51]
	v_mfma_f32_16x16x32_bf16 v[36:39], v[206:209], v[230:233], v[36:39]
	v_mfma_f32_16x16x32_bf16 v[32:35], v[214:217], v[230:233], v[32:35]
	v_mfma_f32_16x16x32_bf16 v[20:23], v[206:209], v[238:241], v[20:23]
	v_mfma_f32_16x16x32_bf16 v[16:19], v[214:217], v[238:241], v[16:19]
	v_mfma_f32_16x16x32_bf16 v[4:7], v[206:209], v[246:249], v[4:7]
	v_mfma_f32_16x16x32_bf16 v[0:3], v[214:217], v[246:249], v[0:3]
	v_mfma_f32_16x16x32_bf16 v[52:55], v[210:213], v[226:229], v[52:55]
	v_mfma_f32_16x16x32_bf16 v[48:51], v[218:221], v[226:229], v[48:51]
	v_mfma_f32_16x16x32_bf16 v[36:39], v[210:213], v[234:237], v[36:39]
	v_mfma_f32_16x16x32_bf16 v[32:35], v[218:221], v[234:237], v[32:35]
	v_mfma_f32_16x16x32_bf16 v[20:23], v[210:213], v[242:245], v[20:23]
	v_mfma_f32_16x16x32_bf16 v[16:19], v[218:221], v[242:245], v[16:19]
	v_mfma_f32_16x16x32_bf16 v[4:7], v[210:213], v[250:253], v[4:7]
	v_mfma_f32_16x16x32_bf16 v[0:3], v[218:221], v[250:253], v[0:3]
	s_setprio 0
	s_barrier
	s_add_i32 s27, s27, 2
	s_add_u32 s50, s50, 0x100
	s_addc_u32 s51, s51, 0
	s_add_u32 s14, s14, 0x100
	s_addc_u32 s15, s15, 0
	s_cmp_gt_u32 s27, 29
	s_cbranch_scc0 .LBB0_2084
	s_and_b64 vcc, exec, s[24:25]
	s_cbranch_vccz .LBB0_2087
	s_barrier

.LBB0_2193:
	s_add_u32 s5, s48, 0xfffc0080
	s_addc_u32 s10, s49, -1
	s_add_i32 s31, 0, 0x10000
	s_cmp_eq_u32 s29, 12
	s_cselect_b32 s53, s45, s10
	s_cselect_b32 s52, s44, s5
	v_add_u32_e32 v144, s31, v146
	s_cselect_b32 s51, s47, s15
	s_cselect_b32 s50, s46, s14
	s_add_i32 s5, 0, 0x14000
	ds_read_b128 v[140:143], v144
	ds_read_b128 v[150:153], v144 offset:1024
	ds_read_b128 v[154:157], v144 offset:2048
	ds_read_b128 v[158:161], v144 offset:3072
	v_add_u32_e32 v144, s5, v146
	ds_read_b128 v[162:165], v144
	ds_read_b128 v[166:169], v144 offset:1024
	ds_read_b128 v[170:173], v144 offset:2048
	ds_read_b128 v[182:185], v144 offset:3072
	s_add_i32 m0, s59, 0xc000
	ds_read_b128 v[186:189], v149
	ds_read_b128 v[206:209], v149 offset:1024
	ds_read_b128 v[210:213], v149 offset:2048
	ds_read_b128 v[214:217], v149 offset:3072
	ds_read_b128 v[218:221], v149 offset:4096
	ds_read_b128 v[222:225], v149 offset:5120
	ds_read_b128 v[226:229], v149 offset:6144
	ds_read_b128 v[230:233], v149 offset:7168
	global_load_lds_dwordx4 v136, s[48:49]
	s_add_i32 m0, s59, 0xe000
	s_nop 0
	global_load_lds_dwordx4 v138, s[48:49]
	s_waitcnt vmcnt(8)
	s_waitcnt lgkmcnt(0)
	s_barrier
	s_setprio 1
	s_waitcnt lgkmcnt(0)
	v_mfma_f32_16x16x32_bf16 v[124:127], v[140:143], v[186:189], v[124:127]
	v_mfma_f32_16x16x32_bf16 v[120:123], v[154:157], v[186:189], v[120:123]
	v_mfma_f32_16x16x32_bf16 v[108:111], v[140:143], v[210:213], v[108:111]
	v_mfma_f32_16x16x32_bf16 v[104:107], v[154:157], v[210:213], v[104:107]
	v_mfma_f32_16x16x32_bf16 v[92:95], v[140:143], v[218:221], v[92:95]
	v_mfma_f32_16x16x32_bf16 v[88:91], v[154:157], v[218:221], v[88:91]
	v_mfma_f32_16x16x32_bf16 v[76:79], v[140:143], v[226:229], v[76:79]
	v_mfma_f32_16x16x32_bf16 v[72:75], v[154:157], v[226:229], v[72:75]
	v_mfma_f32_16x16x32_bf16 v[124:127], v[150:153], v[206:209], v[124:127]
	v_mfma_f32_16x16x32_bf16 v[120:123], v[158:161], v[206:209], v[120:123]
	v_mfma_f32_16x16x32_bf16 v[108:111], v[150:153], v[214:217], v[108:111]
	v_mfma_f32_16x16x32_bf16 v[104:107], v[158:161], v[214:217], v[104:107]
	v_mfma_f32_16x16x32_bf16 v[92:95], v[150:153], v[222:225], v[92:95]
	v_mfma_f32_16x16x32_bf16 v[88:91], v[158:161], v[222:225], v[88:91]
	v_mfma_f32_16x16x32_bf16 v[76:79], v[150:153], v[230:233], v[76:79]
	v_mfma_f32_16x16x32_bf16 v[72:75], v[158:161], v[230:233], v[72:75]
	v_mfma_f32_16x16x32_bf16 v[116:119], v[162:165], v[186:189], v[116:119]
	v_mfma_f32_16x16x32_bf16 v[112:115], v[170:173], v[186:189], v[112:115]
	v_mfma_f32_16x16x32_bf16 v[100:103], v[162:165], v[210:213], v[100:103]
	v_mfma_f32_16x16x32_bf16 v[96:99], v[170:173], v[210:213], v[96:99]
	v_mfma_f32_16x16x32_bf16 v[84:87], v[162:165], v[218:221], v[84:87]
	v_mfma_f32_16x16x32_bf16 v[80:83], v[170:173], v[218:221], v[80:83]
	v_mfma_f32_16x16x32_bf16 v[68:71], v[162:165], v[226:229], v[68:71]
	v_mfma_f32_16x16x32_bf16 v[64:67], v[170:173], v[226:229], v[64:67]
	v_mfma_f32_16x16x32_bf16 v[116:119], v[166:169], v[206:209], v[116:119]
	v_mfma_f32_16x16x32_bf16 v[112:115], v[182:185], v[206:209], v[112:115]
	v_mfma_f32_16x16x32_bf16 v[100:103], v[166:169], v[214:217], v[100:103]
	v_mfma_f32_16x16x32_bf16 v[96:99], v[182:185], v[214:217], v[96:99]
	v_mfma_f32_16x16x32_bf16 v[84:87], v[166:169], v[222:225], v[84:87]
	v_mfma_f32_16x16x32_bf16 v[80:83], v[182:185], v[222:225], v[80:83]
	v_mfma_f32_16x16x32_bf16 v[68:71], v[166:169], v[230:233], v[68:71]
	v_mfma_f32_16x16x32_bf16 v[64:67], v[182:185], v[230:233], v[64:67]
	s_setprio 0
	s_barrier
	s_add_i32 s10, s31, s58
	s_mov_b32 m0, s10
	ds_read_b128 v[186:189], v149 offset:16384
	ds_read_b128 v[206:209], v149 offset:17408
	ds_read_b128 v[210:213], v149 offset:18432
	ds_read_b128 v[214:217], v149 offset:19456
	ds_read_b128 v[218:221], v149 offset:20480
	ds_read_b128 v[222:225], v149 offset:21504
	ds_read_b128 v[226:229], v149 offset:22528
	ds_read_b128 v[230:233], v149 offset:23552
	global_load_lds_dwordx4 v176, s[50:51]
	s_add_i32 m0, s10, 0x2000
	s_add_u32 s74, s50, 0x40000
	s_addc_u32 s75, s51, 0
	s_add_i32 s5, s5, s58
	global_load_lds_dwordx4 v132, s[50:51]
	s_mov_b32 m0, s5
	s_nop 0
	global_load_lds_dwordx4 v176, s[74:75]
	s_add_i32 m0, s5, 0x2000
	s_nop 0
	global_load_lds_dwordx4 v132, s[74:75]
	s_mov_b32 m0, s59
	s_nop 0
	global_load_lds_dwordx4 v128, s[52:53]
	s_mov_b32 m0, s60
	s_nop 0
	global_load_lds_dwordx4 v130, s[52:53]
	s_waitcnt vmcnt(8)
	s_waitcnt lgkmcnt(0)
	s_barrier
	s_setprio 1
	s_waitcnt lgkmcnt(0)
	v_mfma_f32_16x16x32_bf16 v[60:63], v[140:143], v[186:189], v[60:63]
	v_mfma_f32_16x16x32_bf16 v[56:59], v[154:157], v[186:189], v[56:59]
	v_mfma_f32_16x16x32_bf16 v[44:47], v[140:143], v[210:213], v[44:47]
	v_mfma_f32_16x16x32_bf16 v[40:43], v[154:157], v[210:213], v[40:43]
	v_mfma_f32_16x16x32_bf16 v[28:31], v[140:143], v[218:221], v[28:31]
	v_mfma_f32_16x16x32_bf16 v[24:27], v[154:157], v[218:221], v[24:27]
	v_mfma_f32_16x16x32_bf16 v[12:15], v[140:143], v[226:229], v[12:15]
	v_mfma_f32_16x16x32_bf16 v[8:11], v[154:157], v[226:229], v[8:11]
	v_mfma_f32_16x16x32_bf16 v[60:63], v[150:153], v[206:209], v[60:63]
	v_mfma_f32_16x16x32_bf16 v[56:59], v[158:161], v[206:209], v[56:59]
	v_mfma_f32_16x16x32_bf16 v[44:47], v[150:153], v[214:217], v[44:47]
	v_mfma_f32_16x16x32_bf16 v[40:43], v[158:161], v[214:217], v[40:43]
	v_mfma_f32_16x16x32_bf16 v[28:31], v[150:153], v[222:225], v[28:31]
	v_mfma_f32_16x16x32_bf16 v[24:27], v[158:161], v[222:225], v[24:27]
	v_mfma_f32_16x16x32_bf16 v[12:15], v[150:153], v[230:233], v[12:15]
	v_mfma_f32_16x16x32_bf16 v[8:11], v[158:161], v[230:233], v[8:11]
	v_mfma_f32_16x16x32_bf16 v[52:55], v[162:165], v[186:189], v[52:55]
	v_mfma_f32_16x16x32_bf16 v[48:51], v[170:173], v[186:189], v[48:51]
	v_mfma_f32_16x16x32_bf16 v[36:39], v[162:165], v[210:213], v[36:39]
	v_mfma_f32_16x16x32_bf16 v[32:35], v[170:173], v[210:213], v[32:35]
	v_mfma_f32_16x16x32_bf16 v[20:23], v[162:165], v[218:221], v[20:23]
	v_mfma_f32_16x16x32_bf16 v[16:19], v[170:173], v[218:221], v[16:19]
	v_mfma_f32_16x16x32_bf16 v[4:7], v[162:165], v[226:229], v[4:7]
	v_mfma_f32_16x16x32_bf16 v[0:3], v[170:173], v[226:229], v[0:3]
	v_mfma_f32_16x16x32_bf16 v[52:55], v[166:169], v[206:209], v[52:55]
	v_mfma_f32_16x16x32_bf16 v[48:51], v[182:185], v[206:209], v[48:51]
	v_mfma_f32_16x16x32_bf16 v[36:39], v[166:169], v[214:217], v[36:39]
	v_mfma_f32_16x16x32_bf16 v[32:35], v[182:185], v[214:217], v[32:35]
	v_mfma_f32_16x16x32_bf16 v[20:23], v[166:169], v[222:225], v[20:23]
	v_mfma_f32_16x16x32_bf16 v[16:19], v[182:185], v[222:225], v[16:19]
	v_mfma_f32_16x16x32_bf16 v[4:7], v[166:169], v[230:233], v[4:7]
	v_mfma_f32_16x16x32_bf16 v[0:3], v[182:185], v[230:233], v[0:3]
	s_setprio 0
	s_barrier
	s_add_i32 s5, 0, 0x18000
	s_add_i32 s10, 0, 0x1c000
	v_add_u32_e32 v158, s5, v146
	v_add_u32_e32 v182, s10, v146
	ds_read_b128 v[140:143], v158
	ds_read_b128 v[150:153], v158 offset:1024
	ds_read_b128 v[154:157], v158 offset:2048
	ds_read_b128 v[158:161], v158 offset:3072
	ds_read_b128 v[162:165], v182
	ds_read_b128 v[166:169], v182 offset:1024
	ds_read_b128 v[170:173], v182 offset:2048
	ds_read_b128 v[182:185], v182 offset:3072
	s_add_u32 s52, s52, 0x40000
	s_addc_u32 s53, s53, 0
	s_mov_b32 m0, s61
	ds_read_b128 v[186:189], v149 offset:32768
	ds_read_b128 v[206:209], v149 offset:33792
	ds_read_b128 v[210:213], v149 offset:34816
	ds_read_b128 v[214:217], v149 offset:35840
	ds_read_b128 v[218:221], v149 offset:36864
	ds_read_b128 v[222:225], v149 offset:37888
	ds_read_b128 v[226:229], v149 offset:38912
	ds_read_b128 v[230:233], v149 offset:39936
	global_load_lds_dwordx4 v128, s[52:53]
	s_mov_b32 m0, s62
	s_nop 0
	global_load_lds_dwordx4 v130, s[52:53]
	s_waitcnt vmcnt(8)
	s_waitcnt lgkmcnt(0)
	s_barrier
	s_setprio 1
	s_waitcnt lgkmcnt(0)
	v_mfma_f32_16x16x32_bf16 v[124:127], v[140:143], v[186:189], v[124:127]
	v_mfma_f32_16x16x32_bf16 v[120:123], v[154:157], v[186:189], v[120:123]
	v_mfma_f32_16x16x32_bf16 v[108:111], v[140:143], v[210:213], v[108:111]
	v_mfma_f32_16x16x32_bf16 v[104:107], v[154:157], v[210:213], v[104:107]
	v_mfma_f32_16x16x32_bf16 v[92:95], v[140:143], v[218:221], v[92:95]
	v_mfma_f32_16x16x32_bf16 v[88:91], v[154:157], v[218:221], v[88:91]
	v_mfma_f32_16x16x32_bf16 v[76:79], v[140:143], v[226:229], v[76:79]
	v_mfma_f32_16x16x32_bf16 v[72:75], v[154:157], v[226:229], v[72:75]
	v_mfma_f32_16x16x32_bf16 v[124:127], v[150:153], v[206:209], v[124:127]
	v_mfma_f32_16x16x32_bf16 v[120:123], v[158:161], v[206:209], v[120:123]
	v_mfma_f32_16x16x32_bf16 v[108:111], v[150:153], v[214:217], v[108:111]
	v_mfma_f32_16x16x32_bf16 v[104:107], v[158:161], v[214:217], v[104:107]
	v_mfma_f32_16x16x32_bf16 v[92:95], v[150:153], v[222:225], v[92:95]
	v_mfma_f32_16x16x32_bf16 v[88:91], v[158:161], v[222:225], v[88:91]
	v_mfma_f32_16x16x32_bf16 v[76:79], v[150:153], v[230:233], v[76:79]
	v_mfma_f32_16x16x32_bf16 v[72:75], v[158:161], v[230:233], v[72:75]
	v_mfma_f32_16x16x32_bf16 v[116:119], v[162:165], v[186:189], v[116:119]
	v_mfma_f32_16x16x32_bf16 v[112:115], v[170:173], v[186:189], v[112:115]
	v_mfma_f32_16x16x32_bf16 v[100:103], v[162:165], v[210:213], v[100:103]
	v_mfma_f32_16x16x32_bf16 v[96:99], v[170:173], v[210:213], v[96:99]
	v_mfma_f32_16x16x32_bf16 v[84:87], v[162:165], v[218:221], v[84:87]
	v_mfma_f32_16x16x32_bf16 v[80:83], v[170:173], v[218:221], v[80:83]
	v_mfma_f32_16x16x32_bf16 v[68:71], v[162:165], v[226:229], v[68:71]
	v_mfma_f32_16x16x32_bf16 v[64:67], v[170:173], v[226:229], v[64:67]
	v_mfma_f32_16x16x32_bf16 v[116:119], v[166:169], v[206:209], v[116:119]
	v_mfma_f32_16x16x32_bf16 v[112:115], v[182:185], v[206:209], v[112:115]
	v_mfma_f32_16x16x32_bf16 v[100:103], v[166:169], v[214:217], v[100:103]
	v_mfma_f32_16x16x32_bf16 v[96:99], v[182:185], v[214:217], v[96:99]
	v_mfma_f32_16x16x32_bf16 v[84:87], v[166:169], v[222:225], v[84:87]
	v_mfma_f32_16x16x32_bf16 v[80:83], v[182:185], v[222:225], v[80:83]
	v_mfma_f32_16x16x32_bf16 v[68:71], v[166:169], v[230:233], v[68:71]
	v_mfma_f32_16x16x32_bf16 v[64:67], v[182:185], v[230:233], v[64:67]
	s_setprio 0
	s_barrier
	s_add_i32 s5, s5, s58
	s_mov_b32 m0, s5
	ds_read_b128 v[186:189], v149 offset:49152
	ds_read_b128 v[206:209], v149 offset:50176
	ds_read_b128 v[210:213], v149 offset:51200
	ds_read_b128 v[214:217], v149 offset:52224
	ds_read_b128 v[218:221], v149 offset:53248
	ds_read_b128 v[222:225], v149 offset:54272
	ds_read_b128 v[226:229], v149 offset:55296
	ds_read_b128 v[230:233], v149 offset:56320
	s_add_u32 s74, s50, 0x80
	s_addc_u32 s75, s51, 0
	global_load_lds_dwordx4 v176, s[74:75]
	s_add_i32 m0, s5, 0x2000
	s_add_u32 s50, s50, 0x40080
	s_addc_u32 s51, s51, 0
	s_add_i32 s5, s10, s58
	s_add_u32 s74, s50, 0xfffc0000
	s_addc_u32 s75, s51, -1
	global_load_lds_dwordx4 v132, s[74:75]
	s_mov_b32 m0, s5
	s_nop 0
	global_load_lds_dwordx4 v176, s[50:51]
	s_add_i32 m0, s5, 0x2000
	s_nop 0
	global_load_lds_dwordx4 v132, s[50:51]
	s_mov_b32 m0, s64
	s_nop 0
	s_add_u32 s74, s52, 0xfffc0080
	s_addc_u32 s75, s53, -1
	global_load_lds_dwordx4 v128, s[74:75]
	s_mov_b32 m0, s65
	s_nop 0
	s_add_u32 s74, s52, 0xfffc0080
	s_addc_u32 s75, s53, -1
	global_load_lds_dwordx4 v130, s[74:75]
	s_waitcnt vmcnt(8)
	s_waitcnt lgkmcnt(0)
	s_barrier
	s_setprio 1
	s_waitcnt lgkmcnt(0)
	v_mfma_f32_16x16x32_bf16 v[60:63], v[140:143], v[186:189], v[60:63]
	v_mfma_f32_16x16x32_bf16 v[56:59], v[154:157], v[186:189], v[56:59]
	v_mfma_f32_16x16x32_bf16 v[44:47], v[140:143], v[210:213], v[44:47]
	v_mfma_f32_16x16x32_bf16 v[40:43], v[154:157], v[210:213], v[40:43]
	v_mfma_f32_16x16x32_bf16 v[28:31], v[140:143], v[218:221], v[28:31]
	v_mfma_f32_16x16x32_bf16 v[24:27], v[154:157], v[218:221], v[24:27]
	v_mfma_f32_16x16x32_bf16 v[12:15], v[140:143], v[226:229], v[12:15]
	v_mfma_f32_16x16x32_bf16 v[8:11], v[154:157], v[226:229], v[8:11]
	v_mfma_f32_16x16x32_bf16 v[60:63], v[150:153], v[206:209], v[60:63]
	v_mfma_f32_16x16x32_bf16 v[56:59], v[158:161], v[206:209], v[56:59]
	v_mfma_f32_16x16x32_bf16 v[44:47], v[150:153], v[214:217], v[44:47]
	v_mfma_f32_16x16x32_bf16 v[40:43], v[158:161], v[214:217], v[40:43]
	v_mfma_f32_16x16x32_bf16 v[28:31], v[150:153], v[222:225], v[28:31]
	v_mfma_f32_16x16x32_bf16 v[24:27], v[158:161], v[222:225], v[24:27]
	v_mfma_f32_16x16x32_bf16 v[12:15], v[150:153], v[230:233], v[12:15]
	v_mfma_f32_16x16x32_bf16 v[8:11], v[158:161], v[230:233], v[8:11]
	v_mfma_f32_16x16x32_bf16 v[52:55], v[162:165], v[186:189], v[52:55]
	v_mfma_f32_16x16x32_bf16 v[48:51], v[170:173], v[186:189], v[48:51]
	v_mfma_f32_16x16x32_bf16 v[36:39], v[162:165], v[210:213], v[36:39]
	v_mfma_f32_16x16x32_bf16 v[32:35], v[170:173], v[210:213], v[32:35]
	v_mfma_f32_16x16x32_bf16 v[20:23], v[162:165], v[218:221], v[20:23]
	v_mfma_f32_16x16x32_bf16 v[16:19], v[170:173], v[218:221], v[16:19]
	v_mfma_f32_16x16x32_bf16 v[4:7], v[162:165], v[226:229], v[4:7]
	v_mfma_f32_16x16x32_bf16 v[0:3], v[170:173], v[226:229], v[0:3]
	v_mfma_f32_16x16x32_bf16 v[52:55], v[166:169], v[206:209], v[52:55]
	v_mfma_f32_16x16x32_bf16 v[48:51], v[182:185], v[206:209], v[48:51]
	v_mfma_f32_16x16x32_bf16 v[36:39], v[166:169], v[214:217], v[36:39]
	v_mfma_f32_16x16x32_bf16 v[32:35], v[182:185], v[214:217], v[32:35]
	v_mfma_f32_16x16x32_bf16 v[20:23], v[166:169], v[222:225], v[20:23]
	v_mfma_f32_16x16x32_bf16 v[16:19], v[182:185], v[222:225], v[16:19]
	v_mfma_f32_16x16x32_bf16 v[4:7], v[166:169], v[230:233], v[4:7]
	v_mfma_f32_16x16x32_bf16 v[0:3], v[182:185], v[230:233], v[0:3]
	s_setprio 0
	s_barrier
	s_add_i32 s29, s29, 2
	s_add_u32 s48, s48, 0x100
	s_addc_u32 s49, s49, 0
	s_add_u32 s14, s14, 0x100
	s_addc_u32 s15, s15, 0
	s_cmp_gt_u32 s29, 13
	s_cbranch_scc0 .LBB0_2193
	s_and_b64 vcc, exec, s[26:27]
	s_cbranch_vccz .LBB0_2196
	s_barrier

.LBB0_2282:
	s_add_u32 s5, s46, 0xfff80080
	s_addc_u32 s10, s47, -1
	s_add_i32 s29, 0, 0x10000
	s_cmp_eq_u32 s27, 28
	s_cselect_b32 s51, s43, s10
	s_cselect_b32 s50, s42, s5
	v_add_u32_e32 v169, s29, v155
	s_cselect_b32 s49, s45, s15
	s_cselect_b32 s48, s44, s14
	s_add_i32 s5, 0, 0x14000
	ds_read_b128 v[142:145], v169
	ds_read_b128 v[146:149], v169 offset:1024
	ds_read_b128 v[150:153], v169 offset:2048
	ds_read_b128 v[170:173], v169 offset:3072
	v_add_u32_e32 v169, s5, v155
	ds_read_b128 v[182:185], v169
	ds_read_b128 v[186:189], v169 offset:1024
	ds_read_b128 v[206:209], v169 offset:2048
	ds_read_b128 v[210:213], v169 offset:3072
	s_add_i32 m0, s57, 0xc000
	ds_read_b128 v[214:217], v168
	ds_read_b128 v[218:221], v168 offset:1024
	ds_read_b128 v[222:225], v168 offset:2048
	ds_read_b128 v[226:229], v168 offset:3072
	ds_read_b128 v[230:233], v168 offset:4096
	ds_read_b128 v[234:237], v168 offset:5120
	ds_read_b128 v[238:241], v168 offset:6144
	ds_read_b128 v[242:245], v168 offset:7168
	global_load_lds_dwordx4 v138, s[46:47]
	s_add_i32 m0, s57, 0xe000
	s_nop 0
	global_load_lds_dwordx4 v140, s[46:47]
	s_waitcnt vmcnt(8)
	s_waitcnt lgkmcnt(0)
	s_barrier
	s_setprio 1
	s_waitcnt lgkmcnt(0)
	v_mfma_f32_16x16x32_bf16 v[124:127], v[142:145], v[214:217], v[124:127]
	v_mfma_f32_16x16x32_bf16 v[120:123], v[150:153], v[214:217], v[120:123]
	v_mfma_f32_16x16x32_bf16 v[108:111], v[142:145], v[222:225], v[108:111]
	v_mfma_f32_16x16x32_bf16 v[104:107], v[150:153], v[222:225], v[104:107]
	v_mfma_f32_16x16x32_bf16 v[92:95], v[142:145], v[230:233], v[92:95]
	v_mfma_f32_16x16x32_bf16 v[88:91], v[150:153], v[230:233], v[88:91]
	v_mfma_f32_16x16x32_bf16 v[76:79], v[142:145], v[238:241], v[76:79]
	v_mfma_f32_16x16x32_bf16 v[72:75], v[150:153], v[238:241], v[72:75]
	v_mfma_f32_16x16x32_bf16 v[124:127], v[146:149], v[218:221], v[124:127]
	v_mfma_f32_16x16x32_bf16 v[120:123], v[170:173], v[218:221], v[120:123]
	v_mfma_f32_16x16x32_bf16 v[108:111], v[146:149], v[226:229], v[108:111]
	v_mfma_f32_16x16x32_bf16 v[104:107], v[170:173], v[226:229], v[104:107]
	v_mfma_f32_16x16x32_bf16 v[92:95], v[146:149], v[234:237], v[92:95]
	v_mfma_f32_16x16x32_bf16 v[88:91], v[170:173], v[234:237], v[88:91]
	v_mfma_f32_16x16x32_bf16 v[76:79], v[146:149], v[242:245], v[76:79]
	v_mfma_f32_16x16x32_bf16 v[72:75], v[170:173], v[242:245], v[72:75]
	v_mfma_f32_16x16x32_bf16 v[116:119], v[182:185], v[214:217], v[116:119]
	v_mfma_f32_16x16x32_bf16 v[112:115], v[206:209], v[214:217], v[112:115]
	v_mfma_f32_16x16x32_bf16 v[100:103], v[182:185], v[222:225], v[100:103]
	v_mfma_f32_16x16x32_bf16 v[96:99], v[206:209], v[222:225], v[96:99]
	v_mfma_f32_16x16x32_bf16 v[84:87], v[182:185], v[230:233], v[84:87]
	v_mfma_f32_16x16x32_bf16 v[80:83], v[206:209], v[230:233], v[80:83]
	v_mfma_f32_16x16x32_bf16 v[68:71], v[182:185], v[238:241], v[68:71]
	v_mfma_f32_16x16x32_bf16 v[64:67], v[206:209], v[238:241], v[64:67]
	v_mfma_f32_16x16x32_bf16 v[116:119], v[186:189], v[218:221], v[116:119]
	v_mfma_f32_16x16x32_bf16 v[112:115], v[210:213], v[218:221], v[112:115]
	v_mfma_f32_16x16x32_bf16 v[100:103], v[186:189], v[226:229], v[100:103]
	v_mfma_f32_16x16x32_bf16 v[96:99], v[210:213], v[226:229], v[96:99]
	v_mfma_f32_16x16x32_bf16 v[84:87], v[186:189], v[234:237], v[84:87]
	v_mfma_f32_16x16x32_bf16 v[80:83], v[210:213], v[234:237], v[80:83]
	v_mfma_f32_16x16x32_bf16 v[68:71], v[186:189], v[242:245], v[68:71]
	v_mfma_f32_16x16x32_bf16 v[64:67], v[210:213], v[242:245], v[64:67]
	s_setprio 0
	s_barrier
	s_add_i32 s10, s29, s56
	s_mov_b32 m0, s10
	ds_read_b128 v[214:217], v168 offset:16384
	ds_read_b128 v[218:221], v168 offset:17408
	ds_read_b128 v[222:225], v168 offset:18432
	ds_read_b128 v[226:229], v168 offset:19456
	ds_read_b128 v[230:233], v168 offset:20480
	ds_read_b128 v[234:237], v168 offset:21504
	ds_read_b128 v[238:241], v168 offset:22528
	ds_read_b128 v[242:245], v168 offset:23552
	global_load_lds_dwordx4 v130, s[48:49]
	s_add_i32 m0, s10, 0x2000
	s_add_u32 s64, s48, 0x80000
	s_addc_u32 s65, s49, 0
	s_add_i32 s5, s5, s56
	global_load_lds_dwordx4 v134, s[48:49]
	s_mov_b32 m0, s5
	s_nop 0
	global_load_lds_dwordx4 v130, s[64:65]
	s_add_i32 m0, s5, 0x2000
	s_nop 0
	global_load_lds_dwordx4 v134, s[64:65]
	s_mov_b32 m0, s57
	s_nop 0
	global_load_lds_dwordx4 v128, s[50:51]
	s_mov_b32 m0, s58
	s_nop 0
	global_load_lds_dwordx4 v132, s[50:51]
	s_waitcnt vmcnt(8)
	s_waitcnt lgkmcnt(0)
	s_barrier
	s_setprio 1
	s_waitcnt lgkmcnt(0)
	v_mfma_f32_16x16x32_bf16 v[60:63], v[142:145], v[214:217], v[60:63]
	v_mfma_f32_16x16x32_bf16 v[56:59], v[150:153], v[214:217], v[56:59]
	v_mfma_f32_16x16x32_bf16 v[44:47], v[142:145], v[222:225], v[44:47]
	v_mfma_f32_16x16x32_bf16 v[40:43], v[150:153], v[222:225], v[40:43]
	v_mfma_f32_16x16x32_bf16 v[28:31], v[142:145], v[230:233], v[28:31]
	v_mfma_f32_16x16x32_bf16 v[24:27], v[150:153], v[230:233], v[24:27]
	v_mfma_f32_16x16x32_bf16 v[12:15], v[142:145], v[238:241], v[12:15]
	v_mfma_f32_16x16x32_bf16 v[8:11], v[150:153], v[238:241], v[8:11]
	v_mfma_f32_16x16x32_bf16 v[60:63], v[146:149], v[218:221], v[60:63]
	v_mfma_f32_16x16x32_bf16 v[56:59], v[170:173], v[218:221], v[56:59]
	v_mfma_f32_16x16x32_bf16 v[44:47], v[146:149], v[226:229], v[44:47]
	v_mfma_f32_16x16x32_bf16 v[40:43], v[170:173], v[226:229], v[40:43]
	v_mfma_f32_16x16x32_bf16 v[28:31], v[146:149], v[234:237], v[28:31]
	v_mfma_f32_16x16x32_bf16 v[24:27], v[170:173], v[234:237], v[24:27]
	v_mfma_f32_16x16x32_bf16 v[12:15], v[146:149], v[242:245], v[12:15]
	v_mfma_f32_16x16x32_bf16 v[8:11], v[170:173], v[242:245], v[8:11]
	v_mfma_f32_16x16x32_bf16 v[52:55], v[182:185], v[214:217], v[52:55]
	v_mfma_f32_16x16x32_bf16 v[48:51], v[206:209], v[214:217], v[48:51]
	v_mfma_f32_16x16x32_bf16 v[36:39], v[182:185], v[222:225], v[36:39]
	v_mfma_f32_16x16x32_bf16 v[32:35], v[206:209], v[222:225], v[32:35]
	v_mfma_f32_16x16x32_bf16 v[20:23], v[182:185], v[230:233], v[20:23]
	v_mfma_f32_16x16x32_bf16 v[16:19], v[206:209], v[230:233], v[16:19]
	v_mfma_f32_16x16x32_bf16 v[4:7], v[182:185], v[238:241], v[4:7]
	v_mfma_f32_16x16x32_bf16 v[0:3], v[206:209], v[238:241], v[0:3]
	v_mfma_f32_16x16x32_bf16 v[52:55], v[186:189], v[218:221], v[52:55]
	v_mfma_f32_16x16x32_bf16 v[48:51], v[210:213], v[218:221], v[48:51]
	v_mfma_f32_16x16x32_bf16 v[36:39], v[186:189], v[226:229], v[36:39]
	v_mfma_f32_16x16x32_bf16 v[32:35], v[210:213], v[226:229], v[32:35]
	v_mfma_f32_16x16x32_bf16 v[20:23], v[186:189], v[234:237], v[20:23]
	v_mfma_f32_16x16x32_bf16 v[16:19], v[210:213], v[234:237], v[16:19]
	v_mfma_f32_16x16x32_bf16 v[4:7], v[186:189], v[242:245], v[4:7]
	v_mfma_f32_16x16x32_bf16 v[0:3], v[210:213], v[242:245], v[0:3]
	s_setprio 0
	s_barrier
	s_add_i32 s5, 0, 0x18000
	v_add_u32_e32 v169, s5, v155
	s_add_i32 s10, 0, 0x1c000
	ds_read_b128 v[142:145], v169
	ds_read_b128 v[146:149], v169 offset:1024
	ds_read_b128 v[150:153], v169 offset:2048
	ds_read_b128 v[170:173], v169 offset:3072
	v_add_u32_e32 v169, s10, v155
	ds_read_b128 v[182:185], v169
	ds_read_b128 v[186:189], v169 offset:1024
	ds_read_b128 v[206:209], v169 offset:2048
	ds_read_b128 v[210:213], v169 offset:3072
	s_add_u32 s50, s50, 0x80000
	s_addc_u32 s51, s51, 0
	s_mov_b32 m0, s59
	ds_read_b128 v[214:217], v168 offset:32768
	ds_read_b128 v[218:221], v168 offset:33792
	ds_read_b128 v[222:225], v168 offset:34816
	ds_read_b128 v[226:229], v168 offset:35840
	ds_read_b128 v[230:233], v168 offset:36864
	ds_read_b128 v[234:237], v168 offset:37888
	ds_read_b128 v[238:241], v168 offset:38912
	ds_read_b128 v[242:245], v168 offset:39936
	global_load_lds_dwordx4 v128, s[50:51]
	s_mov_b32 m0, s60
	s_nop 0
	global_load_lds_dwordx4 v132, s[50:51]
	s_waitcnt vmcnt(8)
	s_waitcnt lgkmcnt(0)
	s_barrier
	s_setprio 1
	s_waitcnt lgkmcnt(0)
	v_mfma_f32_16x16x32_bf16 v[124:127], v[142:145], v[214:217], v[124:127]
	v_mfma_f32_16x16x32_bf16 v[120:123], v[150:153], v[214:217], v[120:123]
	v_mfma_f32_16x16x32_bf16 v[108:111], v[142:145], v[222:225], v[108:111]
	v_mfma_f32_16x16x32_bf16 v[104:107], v[150:153], v[222:225], v[104:107]
	v_mfma_f32_16x16x32_bf16 v[92:95], v[142:145], v[230:233], v[92:95]
	v_mfma_f32_16x16x32_bf16 v[88:91], v[150:153], v[230:233], v[88:91]
	v_mfma_f32_16x16x32_bf16 v[76:79], v[142:145], v[238:241], v[76:79]
	v_mfma_f32_16x16x32_bf16 v[72:75], v[150:153], v[238:241], v[72:75]
	v_mfma_f32_16x16x32_bf16 v[124:127], v[146:149], v[218:221], v[124:127]
	v_mfma_f32_16x16x32_bf16 v[120:123], v[170:173], v[218:221], v[120:123]
	v_mfma_f32_16x16x32_bf16 v[108:111], v[146:149], v[226:229], v[108:111]
	v_mfma_f32_16x16x32_bf16 v[104:107], v[170:173], v[226:229], v[104:107]
	v_mfma_f32_16x16x32_bf16 v[92:95], v[146:149], v[234:237], v[92:95]
	v_mfma_f32_16x16x32_bf16 v[88:91], v[170:173], v[234:237], v[88:91]
	v_mfma_f32_16x16x32_bf16 v[76:79], v[146:149], v[242:245], v[76:79]
	v_mfma_f32_16x16x32_bf16 v[72:75], v[170:173], v[242:245], v[72:75]
	v_mfma_f32_16x16x32_bf16 v[116:119], v[182:185], v[214:217], v[116:119]
	v_mfma_f32_16x16x32_bf16 v[112:115], v[206:209], v[214:217], v[112:115]
	v_mfma_f32_16x16x32_bf16 v[100:103], v[182:185], v[222:225], v[100:103]
	v_mfma_f32_16x16x32_bf16 v[96:99], v[206:209], v[222:225], v[96:99]
	v_mfma_f32_16x16x32_bf16 v[84:87], v[182:185], v[230:233], v[84:87]
	v_mfma_f32_16x16x32_bf16 v[80:83], v[206:209], v[230:233], v[80:83]
	v_mfma_f32_16x16x32_bf16 v[68:71], v[182:185], v[238:241], v[68:71]
	v_mfma_f32_16x16x32_bf16 v[64:67], v[206:209], v[238:241], v[64:67]
	v_mfma_f32_16x16x32_bf16 v[116:119], v[186:189], v[218:221], v[116:119]
	v_mfma_f32_16x16x32_bf16 v[112:115], v[210:213], v[218:221], v[112:115]
	v_mfma_f32_16x16x32_bf16 v[100:103], v[186:189], v[226:229], v[100:103]
	v_mfma_f32_16x16x32_bf16 v[96:99], v[210:213], v[226:229], v[96:99]
	v_mfma_f32_16x16x32_bf16 v[84:87], v[186:189], v[234:237], v[84:87]
	v_mfma_f32_16x16x32_bf16 v[80:83], v[210:213], v[234:237], v[80:83]
	v_mfma_f32_16x16x32_bf16 v[68:71], v[186:189], v[242:245], v[68:71]
	v_mfma_f32_16x16x32_bf16 v[64:67], v[210:213], v[242:245], v[64:67]
	s_setprio 0
	s_barrier
	s_add_i32 s5, s5, s56
	s_mov_b32 m0, s5
	ds_read_b128 v[214:217], v168 offset:49152
	ds_read_b128 v[218:221], v168 offset:50176
	ds_read_b128 v[222:225], v168 offset:51200
	ds_read_b128 v[226:229], v168 offset:52224
	ds_read_b128 v[230:233], v168 offset:53248
	ds_read_b128 v[234:237], v168 offset:54272
	ds_read_b128 v[238:241], v168 offset:55296
	ds_read_b128 v[242:245], v168 offset:56320
	s_add_u32 s64, s48, 0x80
	s_addc_u32 s65, s49, 0
	global_load_lds_dwordx4 v130, s[64:65]
	s_add_i32 m0, s5, 0x2000
	s_add_u32 s48, s48, 0x80080
	s_addc_u32 s49, s49, 0
	s_add_i32 s5, s10, s56
	s_add_u32 s64, s48, 0xfff80000
	s_addc_u32 s65, s49, -1
	global_load_lds_dwordx4 v134, s[64:65]
	s_mov_b32 m0, s5
	s_nop 0
	global_load_lds_dwordx4 v130, s[48:49]
	s_add_i32 m0, s5, 0x2000
	s_nop 0
	global_load_lds_dwordx4 v134, s[48:49]
	s_mov_b32 m0, s61
	s_nop 0
	s_add_u32 s64, s50, 0xfff80080
	s_addc_u32 s65, s51, -1
	global_load_lds_dwordx4 v128, s[64:65]
	s_mov_b32 m0, s62
	s_nop 0
	s_add_u32 s64, s50, 0xfff80080
	s_addc_u32 s65, s51, -1
	global_load_lds_dwordx4 v132, s[64:65]
	s_waitcnt vmcnt(8)
	s_waitcnt lgkmcnt(0)
	s_barrier
	s_setprio 1
	s_waitcnt lgkmcnt(0)
	v_mfma_f32_16x16x32_bf16 v[60:63], v[142:145], v[214:217], v[60:63]
	v_mfma_f32_16x16x32_bf16 v[56:59], v[150:153], v[214:217], v[56:59]
	v_mfma_f32_16x16x32_bf16 v[44:47], v[142:145], v[222:225], v[44:47]
	v_mfma_f32_16x16x32_bf16 v[40:43], v[150:153], v[222:225], v[40:43]
	v_mfma_f32_16x16x32_bf16 v[28:31], v[142:145], v[230:233], v[28:31]
	v_mfma_f32_16x16x32_bf16 v[24:27], v[150:153], v[230:233], v[24:27]
	v_mfma_f32_16x16x32_bf16 v[12:15], v[142:145], v[238:241], v[12:15]
	v_mfma_f32_16x16x32_bf16 v[8:11], v[150:153], v[238:241], v[8:11]
	v_mfma_f32_16x16x32_bf16 v[60:63], v[146:149], v[218:221], v[60:63]
	v_mfma_f32_16x16x32_bf16 v[56:59], v[170:173], v[218:221], v[56:59]
	v_mfma_f32_16x16x32_bf16 v[44:47], v[146:149], v[226:229], v[44:47]
	v_mfma_f32_16x16x32_bf16 v[40:43], v[170:173], v[226:229], v[40:43]
	v_mfma_f32_16x16x32_bf16 v[28:31], v[146:149], v[234:237], v[28:31]
	v_mfma_f32_16x16x32_bf16 v[24:27], v[170:173], v[234:237], v[24:27]
	v_mfma_f32_16x16x32_bf16 v[12:15], v[146:149], v[242:245], v[12:15]
	v_mfma_f32_16x16x32_bf16 v[8:11], v[170:173], v[242:245], v[8:11]
	v_mfma_f32_16x16x32_bf16 v[52:55], v[182:185], v[214:217], v[52:55]
	v_mfma_f32_16x16x32_bf16 v[48:51], v[206:209], v[214:217], v[48:51]
	v_mfma_f32_16x16x32_bf16 v[36:39], v[182:185], v[222:225], v[36:39]
	v_mfma_f32_16x16x32_bf16 v[32:35], v[206:209], v[222:225], v[32:35]
	v_mfma_f32_16x16x32_bf16 v[20:23], v[182:185], v[230:233], v[20:23]
	v_mfma_f32_16x16x32_bf16 v[16:19], v[206:209], v[230:233], v[16:19]
	v_mfma_f32_16x16x32_bf16 v[4:7], v[182:185], v[238:241], v[4:7]
	v_mfma_f32_16x16x32_bf16 v[0:3], v[206:209], v[238:241], v[0:3]
	v_mfma_f32_16x16x32_bf16 v[52:55], v[186:189], v[218:221], v[52:55]
	v_mfma_f32_16x16x32_bf16 v[48:51], v[210:213], v[218:221], v[48:51]
	v_mfma_f32_16x16x32_bf16 v[36:39], v[186:189], v[226:229], v[36:39]
	v_mfma_f32_16x16x32_bf16 v[32:35], v[210:213], v[226:229], v[32:35]
	v_mfma_f32_16x16x32_bf16 v[20:23], v[186:189], v[234:237], v[20:23]
	v_mfma_f32_16x16x32_bf16 v[16:19], v[210:213], v[234:237], v[16:19]
	v_mfma_f32_16x16x32_bf16 v[4:7], v[186:189], v[242:245], v[4:7]
	v_mfma_f32_16x16x32_bf16 v[0:3], v[210:213], v[242:245], v[0:3]
	s_setprio 0
	s_barrier
	s_add_i32 s27, s27, 2
	s_add_u32 s46, s46, 0x100
	s_addc_u32 s47, s47, 0
	s_add_u32 s14, s14, 0x100
	s_addc_u32 s15, s15, 0
	s_cmp_gt_u32 s27, 29
	s_cbranch_scc0 .LBB0_2282
	s_and_b64 vcc, exec, s[24:25]
	s_cbranch_vccz .LBB0_2285
	s_barrier

.LBB0_2357:
	s_add_u32 s5, s48, 0xffe00080
	s_addc_u32 s10, s49, -1
	s_add_i32 s31, 0, 0x10000
	s_cmpk_eq_i32 s29, 0x7c
	s_cselect_b32 s53, s45, s10
	s_cselect_b32 s52, s44, s5
	v_add_u32_e32 v144, s31, v146
	s_cselect_b32 s51, s47, s15
	s_cselect_b32 s50, s46, s14
	s_add_i32 s5, 0, 0x14000
	ds_read_b128 v[140:143], v144
	ds_read_b128 v[150:153], v144 offset:1024
	ds_read_b128 v[154:157], v144 offset:2048
	ds_read_b128 v[158:161], v144 offset:3072
	v_add_u32_e32 v144, s5, v146
	ds_read_b128 v[162:165], v144
	ds_read_b128 v[166:169], v144 offset:1024
	ds_read_b128 v[170:173], v144 offset:2048
	ds_read_b128 v[182:185], v144 offset:3072
	s_add_i32 m0, s59, 0xc000
	ds_read_b128 v[186:189], v149
	ds_read_b128 v[206:209], v149 offset:1024
	ds_read_b128 v[210:213], v149 offset:2048
	ds_read_b128 v[214:217], v149 offset:3072
	ds_read_b128 v[218:221], v149 offset:4096
	ds_read_b128 v[222:225], v149 offset:5120
	ds_read_b128 v[226:229], v149 offset:6144
	ds_read_b128 v[230:233], v149 offset:7168
	global_load_lds_dwordx4 v136, s[48:49]
	s_add_i32 m0, s59, 0xe000
	s_nop 0
	global_load_lds_dwordx4 v138, s[48:49]
	s_waitcnt vmcnt(8)
	s_waitcnt lgkmcnt(0)
	s_barrier
	s_setprio 1
	s_waitcnt lgkmcnt(0)
	v_mfma_f32_16x16x32_bf16 v[124:127], v[140:143], v[186:189], v[124:127]
	v_mfma_f32_16x16x32_bf16 v[120:123], v[154:157], v[186:189], v[120:123]
	v_mfma_f32_16x16x32_bf16 v[108:111], v[140:143], v[210:213], v[108:111]
	v_mfma_f32_16x16x32_bf16 v[104:107], v[154:157], v[210:213], v[104:107]
	v_mfma_f32_16x16x32_bf16 v[92:95], v[140:143], v[218:221], v[92:95]
	v_mfma_f32_16x16x32_bf16 v[88:91], v[154:157], v[218:221], v[88:91]
	v_mfma_f32_16x16x32_bf16 v[76:79], v[140:143], v[226:229], v[76:79]
	v_mfma_f32_16x16x32_bf16 v[72:75], v[154:157], v[226:229], v[72:75]
	v_mfma_f32_16x16x32_bf16 v[124:127], v[150:153], v[206:209], v[124:127]
	v_mfma_f32_16x16x32_bf16 v[120:123], v[158:161], v[206:209], v[120:123]
	v_mfma_f32_16x16x32_bf16 v[108:111], v[150:153], v[214:217], v[108:111]
	v_mfma_f32_16x16x32_bf16 v[104:107], v[158:161], v[214:217], v[104:107]
	v_mfma_f32_16x16x32_bf16 v[92:95], v[150:153], v[222:225], v[92:95]
	v_mfma_f32_16x16x32_bf16 v[88:91], v[158:161], v[222:225], v[88:91]
	v_mfma_f32_16x16x32_bf16 v[76:79], v[150:153], v[230:233], v[76:79]
	v_mfma_f32_16x16x32_bf16 v[72:75], v[158:161], v[230:233], v[72:75]
	v_mfma_f32_16x16x32_bf16 v[116:119], v[162:165], v[186:189], v[116:119]
	v_mfma_f32_16x16x32_bf16 v[112:115], v[170:173], v[186:189], v[112:115]
	v_mfma_f32_16x16x32_bf16 v[100:103], v[162:165], v[210:213], v[100:103]
	v_mfma_f32_16x16x32_bf16 v[96:99], v[170:173], v[210:213], v[96:99]
	v_mfma_f32_16x16x32_bf16 v[84:87], v[162:165], v[218:221], v[84:87]
	v_mfma_f32_16x16x32_bf16 v[80:83], v[170:173], v[218:221], v[80:83]
	v_mfma_f32_16x16x32_bf16 v[68:71], v[162:165], v[226:229], v[68:71]
	v_mfma_f32_16x16x32_bf16 v[64:67], v[170:173], v[226:229], v[64:67]
	v_mfma_f32_16x16x32_bf16 v[116:119], v[166:169], v[206:209], v[116:119]
	v_mfma_f32_16x16x32_bf16 v[112:115], v[182:185], v[206:209], v[112:115]
	v_mfma_f32_16x16x32_bf16 v[100:103], v[166:169], v[214:217], v[100:103]
	v_mfma_f32_16x16x32_bf16 v[96:99], v[182:185], v[214:217], v[96:99]
	v_mfma_f32_16x16x32_bf16 v[84:87], v[166:169], v[222:225], v[84:87]
	v_mfma_f32_16x16x32_bf16 v[80:83], v[182:185], v[222:225], v[80:83]
	v_mfma_f32_16x16x32_bf16 v[68:71], v[166:169], v[230:233], v[68:71]
	v_mfma_f32_16x16x32_bf16 v[64:67], v[182:185], v[230:233], v[64:67]
	s_setprio 0
	s_barrier
	s_add_i32 s10, s31, s58
	s_mov_b32 m0, s10
	ds_read_b128 v[186:189], v149 offset:16384
	ds_read_b128 v[206:209], v149 offset:17408
	ds_read_b128 v[210:213], v149 offset:18432
	ds_read_b128 v[214:217], v149 offset:19456
	ds_read_b128 v[218:221], v149 offset:20480
	ds_read_b128 v[222:225], v149 offset:21504
	ds_read_b128 v[226:229], v149 offset:22528
	ds_read_b128 v[230:233], v149 offset:23552
	global_load_lds_dwordx4 v176, s[50:51]
	s_add_i32 m0, s10, 0x2000
	s_add_u32 s74, s50, 0x200000
	s_addc_u32 s75, s51, 0
	s_add_i32 s5, s5, s58
	global_load_lds_dwordx4 v132, s[50:51]
	s_mov_b32 m0, s5
	s_nop 0
	global_load_lds_dwordx4 v176, s[74:75]
	s_add_i32 m0, s5, 0x2000
	s_nop 0
	global_load_lds_dwordx4 v132, s[74:75]
	s_mov_b32 m0, s59
	s_nop 0
	global_load_lds_dwordx4 v128, s[52:53]
	s_mov_b32 m0, s60
	s_nop 0
	global_load_lds_dwordx4 v130, s[52:53]
	s_waitcnt vmcnt(8)
	s_waitcnt lgkmcnt(0)
	s_barrier
	s_setprio 1
	s_waitcnt lgkmcnt(0)
	v_mfma_f32_16x16x32_bf16 v[60:63], v[140:143], v[186:189], v[60:63]
	v_mfma_f32_16x16x32_bf16 v[56:59], v[154:157], v[186:189], v[56:59]
	v_mfma_f32_16x16x32_bf16 v[44:47], v[140:143], v[210:213], v[44:47]
	v_mfma_f32_16x16x32_bf16 v[40:43], v[154:157], v[210:213], v[40:43]
	v_mfma_f32_16x16x32_bf16 v[28:31], v[140:143], v[218:221], v[28:31]
	v_mfma_f32_16x16x32_bf16 v[24:27], v[154:157], v[218:221], v[24:27]
	v_mfma_f32_16x16x32_bf16 v[12:15], v[140:143], v[226:229], v[12:15]
	v_mfma_f32_16x16x32_bf16 v[8:11], v[154:157], v[226:229], v[8:11]
	v_mfma_f32_16x16x32_bf16 v[60:63], v[150:153], v[206:209], v[60:63]
	v_mfma_f32_16x16x32_bf16 v[56:59], v[158:161], v[206:209], v[56:59]
	v_mfma_f32_16x16x32_bf16 v[44:47], v[150:153], v[214:217], v[44:47]
	v_mfma_f32_16x16x32_bf16 v[40:43], v[158:161], v[214:217], v[40:43]
	v_mfma_f32_16x16x32_bf16 v[28:31], v[150:153], v[222:225], v[28:31]
	v_mfma_f32_16x16x32_bf16 v[24:27], v[158:161], v[222:225], v[24:27]
	v_mfma_f32_16x16x32_bf16 v[12:15], v[150:153], v[230:233], v[12:15]
	v_mfma_f32_16x16x32_bf16 v[8:11], v[158:161], v[230:233], v[8:11]
	v_mfma_f32_16x16x32_bf16 v[52:55], v[162:165], v[186:189], v[52:55]
	v_mfma_f32_16x16x32_bf16 v[48:51], v[170:173], v[186:189], v[48:51]
	v_mfma_f32_16x16x32_bf16 v[36:39], v[162:165], v[210:213], v[36:39]
	v_mfma_f32_16x16x32_bf16 v[32:35], v[170:173], v[210:213], v[32:35]
	v_mfma_f32_16x16x32_bf16 v[20:23], v[162:165], v[218:221], v[20:23]
	v_mfma_f32_16x16x32_bf16 v[16:19], v[170:173], v[218:221], v[16:19]
	v_mfma_f32_16x16x32_bf16 v[4:7], v[162:165], v[226:229], v[4:7]
	v_mfma_f32_16x16x32_bf16 v[0:3], v[170:173], v[226:229], v[0:3]
	v_mfma_f32_16x16x32_bf16 v[52:55], v[166:169], v[206:209], v[52:55]
	v_mfma_f32_16x16x32_bf16 v[48:51], v[182:185], v[206:209], v[48:51]
	v_mfma_f32_16x16x32_bf16 v[36:39], v[166:169], v[214:217], v[36:39]
	v_mfma_f32_16x16x32_bf16 v[32:35], v[182:185], v[214:217], v[32:35]
	v_mfma_f32_16x16x32_bf16 v[20:23], v[166:169], v[222:225], v[20:23]
	v_mfma_f32_16x16x32_bf16 v[16:19], v[182:185], v[222:225], v[16:19]
	v_mfma_f32_16x16x32_bf16 v[4:7], v[166:169], v[230:233], v[4:7]
	v_mfma_f32_16x16x32_bf16 v[0:3], v[182:185], v[230:233], v[0:3]
	s_setprio 0
	s_barrier
	s_add_i32 s5, 0, 0x18000
	s_add_i32 s10, 0, 0x1c000
	v_add_u32_e32 v158, s5, v146
	v_add_u32_e32 v182, s10, v146
	ds_read_b128 v[140:143], v158
	ds_read_b128 v[150:153], v158 offset:1024
	ds_read_b128 v[154:157], v158 offset:2048
	ds_read_b128 v[158:161], v158 offset:3072
	ds_read_b128 v[162:165], v182
	ds_read_b128 v[166:169], v182 offset:1024
	ds_read_b128 v[170:173], v182 offset:2048
	ds_read_b128 v[182:185], v182 offset:3072
	s_add_u32 s52, s52, 0x200000
	s_addc_u32 s53, s53, 0
	s_mov_b32 m0, s61
	ds_read_b128 v[186:189], v149 offset:32768
	ds_read_b128 v[206:209], v149 offset:33792
	ds_read_b128 v[210:213], v149 offset:34816
	ds_read_b128 v[214:217], v149 offset:35840
	ds_read_b128 v[218:221], v149 offset:36864
	ds_read_b128 v[222:225], v149 offset:37888
	ds_read_b128 v[226:229], v149 offset:38912
	ds_read_b128 v[230:233], v149 offset:39936
	global_load_lds_dwordx4 v128, s[52:53]
	s_mov_b32 m0, s62
	s_nop 0
	global_load_lds_dwordx4 v130, s[52:53]
	s_waitcnt vmcnt(8)
	s_waitcnt lgkmcnt(0)
	s_barrier
	s_setprio 1
	s_waitcnt lgkmcnt(0)
	v_mfma_f32_16x16x32_bf16 v[124:127], v[140:143], v[186:189], v[124:127]
	v_mfma_f32_16x16x32_bf16 v[120:123], v[154:157], v[186:189], v[120:123]
	v_mfma_f32_16x16x32_bf16 v[108:111], v[140:143], v[210:213], v[108:111]
	v_mfma_f32_16x16x32_bf16 v[104:107], v[154:157], v[210:213], v[104:107]
	v_mfma_f32_16x16x32_bf16 v[92:95], v[140:143], v[218:221], v[92:95]
	v_mfma_f32_16x16x32_bf16 v[88:91], v[154:157], v[218:221], v[88:91]
	v_mfma_f32_16x16x32_bf16 v[76:79], v[140:143], v[226:229], v[76:79]
	v_mfma_f32_16x16x32_bf16 v[72:75], v[154:157], v[226:229], v[72:75]
	v_mfma_f32_16x16x32_bf16 v[124:127], v[150:153], v[206:209], v[124:127]
	v_mfma_f32_16x16x32_bf16 v[120:123], v[158:161], v[206:209], v[120:123]
	v_mfma_f32_16x16x32_bf16 v[108:111], v[150:153], v[214:217], v[108:111]
	v_mfma_f32_16x16x32_bf16 v[104:107], v[158:161], v[214:217], v[104:107]
	v_mfma_f32_16x16x32_bf16 v[92:95], v[150:153], v[222:225], v[92:95]
	v_mfma_f32_16x16x32_bf16 v[88:91], v[158:161], v[222:225], v[88:91]
	v_mfma_f32_16x16x32_bf16 v[76:79], v[150:153], v[230:233], v[76:79]
	v_mfma_f32_16x16x32_bf16 v[72:75], v[158:161], v[230:233], v[72:75]
	v_mfma_f32_16x16x32_bf16 v[116:119], v[162:165], v[186:189], v[116:119]
	v_mfma_f32_16x16x32_bf16 v[112:115], v[170:173], v[186:189], v[112:115]
	v_mfma_f32_16x16x32_bf16 v[100:103], v[162:165], v[210:213], v[100:103]
	v_mfma_f32_16x16x32_bf16 v[96:99], v[170:173], v[210:213], v[96:99]
	v_mfma_f32_16x16x32_bf16 v[84:87], v[162:165], v[218:221], v[84:87]
	v_mfma_f32_16x16x32_bf16 v[80:83], v[170:173], v[218:221], v[80:83]
	v_mfma_f32_16x16x32_bf16 v[68:71], v[162:165], v[226:229], v[68:71]
	v_mfma_f32_16x16x32_bf16 v[64:67], v[170:173], v[226:229], v[64:67]
	v_mfma_f32_16x16x32_bf16 v[116:119], v[166:169], v[206:209], v[116:119]
	v_mfma_f32_16x16x32_bf16 v[112:115], v[182:185], v[206:209], v[112:115]
	v_mfma_f32_16x16x32_bf16 v[100:103], v[166:169], v[214:217], v[100:103]
	v_mfma_f32_16x16x32_bf16 v[96:99], v[182:185], v[214:217], v[96:99]
	v_mfma_f32_16x16x32_bf16 v[84:87], v[166:169], v[222:225], v[84:87]
	v_mfma_f32_16x16x32_bf16 v[80:83], v[182:185], v[222:225], v[80:83]
	v_mfma_f32_16x16x32_bf16 v[68:71], v[166:169], v[230:233], v[68:71]
	v_mfma_f32_16x16x32_bf16 v[64:67], v[182:185], v[230:233], v[64:67]
	s_setprio 0
	s_barrier
	s_add_i32 s5, s5, s58
	s_mov_b32 m0, s5
	ds_read_b128 v[186:189], v149 offset:49152
	ds_read_b128 v[206:209], v149 offset:50176
	ds_read_b128 v[210:213], v149 offset:51200
	ds_read_b128 v[214:217], v149 offset:52224
	ds_read_b128 v[218:221], v149 offset:53248
	ds_read_b128 v[222:225], v149 offset:54272
	ds_read_b128 v[226:229], v149 offset:55296
	ds_read_b128 v[230:233], v149 offset:56320
	s_add_u32 s74, s50, 0x80
	s_addc_u32 s75, s51, 0
	global_load_lds_dwordx4 v176, s[74:75]
	s_add_i32 m0, s5, 0x2000
	s_add_u32 s50, s50, 0x200080
	s_addc_u32 s51, s51, 0
	s_add_i32 s5, s10, s58
	s_add_u32 s74, s50, 0xffe00000
	s_addc_u32 s75, s51, -1
	global_load_lds_dwordx4 v132, s[74:75]
	s_mov_b32 m0, s5
	s_nop 0
	global_load_lds_dwordx4 v176, s[50:51]
	s_add_i32 m0, s5, 0x2000
	s_nop 0
	global_load_lds_dwordx4 v132, s[50:51]
	s_mov_b32 m0, s64
	s_nop 0
	s_add_u32 s74, s52, 0xffe00080
	s_addc_u32 s75, s53, -1
	global_load_lds_dwordx4 v128, s[74:75]
	s_mov_b32 m0, s65
	s_nop 0
	s_add_u32 s74, s52, 0xffe00080
	s_addc_u32 s75, s53, -1
	global_load_lds_dwordx4 v130, s[74:75]
	s_waitcnt vmcnt(8)
	s_waitcnt lgkmcnt(0)
	s_barrier
	s_setprio 1
	s_waitcnt lgkmcnt(0)
	v_mfma_f32_16x16x32_bf16 v[60:63], v[140:143], v[186:189], v[60:63]
	v_mfma_f32_16x16x32_bf16 v[56:59], v[154:157], v[186:189], v[56:59]
	v_mfma_f32_16x16x32_bf16 v[44:47], v[140:143], v[210:213], v[44:47]
	v_mfma_f32_16x16x32_bf16 v[40:43], v[154:157], v[210:213], v[40:43]
	v_mfma_f32_16x16x32_bf16 v[28:31], v[140:143], v[218:221], v[28:31]
	v_mfma_f32_16x16x32_bf16 v[24:27], v[154:157], v[218:221], v[24:27]
	v_mfma_f32_16x16x32_bf16 v[12:15], v[140:143], v[226:229], v[12:15]
	v_mfma_f32_16x16x32_bf16 v[8:11], v[154:157], v[226:229], v[8:11]
	v_mfma_f32_16x16x32_bf16 v[60:63], v[150:153], v[206:209], v[60:63]
	v_mfma_f32_16x16x32_bf16 v[56:59], v[158:161], v[206:209], v[56:59]
	v_mfma_f32_16x16x32_bf16 v[44:47], v[150:153], v[214:217], v[44:47]
	v_mfma_f32_16x16x32_bf16 v[40:43], v[158:161], v[214:217], v[40:43]
	v_mfma_f32_16x16x32_bf16 v[28:31], v[150:153], v[222:225], v[28:31]
	v_mfma_f32_16x16x32_bf16 v[24:27], v[158:161], v[222:225], v[24:27]
	v_mfma_f32_16x16x32_bf16 v[12:15], v[150:153], v[230:233], v[12:15]
	v_mfma_f32_16x16x32_bf16 v[8:11], v[158:161], v[230:233], v[8:11]
	v_mfma_f32_16x16x32_bf16 v[52:55], v[162:165], v[186:189], v[52:55]
	v_mfma_f32_16x16x32_bf16 v[48:51], v[170:173], v[186:189], v[48:51]
	v_mfma_f32_16x16x32_bf16 v[36:39], v[162:165], v[210:213], v[36:39]
	v_mfma_f32_16x16x32_bf16 v[32:35], v[170:173], v[210:213], v[32:35]
	v_mfma_f32_16x16x32_bf16 v[20:23], v[162:165], v[218:221], v[20:23]
	v_mfma_f32_16x16x32_bf16 v[16:19], v[170:173], v[218:221], v[16:19]
	v_mfma_f32_16x16x32_bf16 v[4:7], v[162:165], v[226:229], v[4:7]
	v_mfma_f32_16x16x32_bf16 v[0:3], v[170:173], v[226:229], v[0:3]
	v_mfma_f32_16x16x32_bf16 v[52:55], v[166:169], v[206:209], v[52:55]
	v_mfma_f32_16x16x32_bf16 v[48:51], v[182:185], v[206:209], v[48:51]
	v_mfma_f32_16x16x32_bf16 v[36:39], v[166:169], v[214:217], v[36:39]
	v_mfma_f32_16x16x32_bf16 v[32:35], v[182:185], v[214:217], v[32:35]
	v_mfma_f32_16x16x32_bf16 v[20:23], v[166:169], v[222:225], v[20:23]
	v_mfma_f32_16x16x32_bf16 v[16:19], v[182:185], v[222:225], v[16:19]
	v_mfma_f32_16x16x32_bf16 v[4:7], v[166:169], v[230:233], v[4:7]
	v_mfma_f32_16x16x32_bf16 v[0:3], v[182:185], v[230:233], v[0:3]
	s_setprio 0
	s_barrier
	s_add_i32 s29, s29, 2
	s_add_u32 s48, s48, 0x100
	s_addc_u32 s49, s49, 0
	s_add_u32 s14, s14, 0x100
	s_addc_u32 s15, s15, 0
	s_cmpk_gt_u32 s29, 0x7d
	s_cbranch_scc0 .LBB0_2357
	s_and_b64 vcc, exec, s[26:27]
	s_cbranch_vccz .LBB0_2360
	s_barrier
